# retention out pass output loop rewritten: gain loads hoisted, saddr addressing, no register shuffles, division without the never-triggered div_scale/div_fmas scaling
# speedup vs baseline: 1.0040x; 1.0040x over previous
; #define LAS __attribute__((address_space(3)))
; __device__ __forceinline__ bf16_t f2bf(float f) { unsigned u = __builtin_bit_cast(unsigned, f); return (bf16_t)((u + 0x7fffu + ((u >> 16) & 1u)) >> 16); }
; __device__ __forceinline__ int crow(int r, int hi) { return (r & 3) + 8 * (r >> 2) + 4 * hi; }
; __device__ __forceinline__ int crow(int r, int hi) { return (r & 3) + 8 * (r >> 2) + 4 * hi; }
; template <int DK, int DV, bool MLSTM>
; __device__ __forceinline__ void out_unit2(LAS unsigned char* lds, LAS unsigned char* ldstab, const OutArgs a, const int wv) {
;     ...
;     __syncthreads();
;     constexpr int TP = DV * 2;
;     static_assert(128 * TP <= 2 * NPK * 32768, "output tile fits the Q + K regions");
; #pragma unroll
;     for (int r = 0; r < 16; ++r) {
;         const int row = 32 * rb + crow(r, hi);
;         const float t1 = s1[r] + exch[((1 - dh) * 128 + row) * 2], t2 = s2[r] + exch[((1 - dh) * 128 + row) * 2 + 1];
;         float mean, inv;
;         if (MLSTM) { mean = 0.f; inv = rsqrtf(t2 * (1.f / DV) + EPS); }
;         else { mean = t1 * (1.f / DV); inv = rsqrtf(fmaxf(t2 * (1.f / DV) - mean * mean, 0.f) + EPS); }
; #pragma unroll
;         for (int nb = 0; nb < NB; ++nb) { const int col = dh * (DV / 2) + 32 * nb + r32;
;             *(LAS bf16_t*)(lds + row * TP + col * 2) = f2bf((o[nb][r] - mean) * inv); }
;     }
.LBB0_1838:
	s_or_b64 exec, exec, s[4:5]
	v_lshlrev_b32_e32 v164, 1, v219
	v_subrev_u32_e32 v164, s6, v164
	s_add_i32 s4, 0, 0x22100
	v_lshl_add_u32 v164, v164, 2, s4
	s_waitcnt vmcnt(0) lgkmcnt(0)
	s_barrier
	ds_read_b128 v[164:167], v164 offset:1024
	v_lshlrev_b32_e32 v168, 1, v217
	v_subrev_u32_e32 v168, s6, v168
	v_lshl_add_u32 v168, v168, 2, s4
	ds_read2_b64 v[168:171], v168 offset0:128 offset1:129
	s_waitcnt lgkmcnt(1)
	v_pk_add_f32 v[156:157], v[156:157], v[164:165]
	s_nop 0
	v_pk_mul_f32 v[156:157], v[156:157], s[36:37] op_sel_hi:[1,0]
	s_nop 0
	v_fma_f32 v157, -v156, v156, v157
	v_max_f32_e32 v157, 0, v157
	v_add_f32_e32 v157, 0x358637bd, v157
	v_mul_f32_e32 v164, 0x4b800000, v157
	v_cmp_gt_f32_e32 vcc, s89, v157
	v_sub_f32_e32 v16, v16, v156
	v_sub_f32_e32 v0, v0, v156
	v_cndmask_b32_e32 v157, v157, v164, vcc
	v_rsq_f32_e32 v157, v157
	v_or_b32_e32 v164, s6, v233
	v_mul_f32_e32 v165, 0x45800000, v157
	v_cndmask_b32_e32 v157, v157, v165, vcc
	v_mul_f32_e32 v16, v16, v157
	v_bfe_u32 v172, v16, 16, 1
	v_lshlrev_b32_e32 v165, 10, v219
	v_add3_u32 v172, v16, v172, s90
	v_lshlrev_b32_e32 v16, 1, v164
	v_mul_f32_e32 v0, v0, v157
	v_add3_u32 v164, 0, v165, v16
	v_bfe_u32 v165, v0, 16, 1
	v_add3_u32 v0, v0, v165, s90
	ds_write_b16_d16_hi v164, v0 offset:64
	v_sub_f32_e32 v0, v32, v156
	v_mul_f32_e32 v0, v0, v157
	v_bfe_u32 v32, v0, 16, 1
	v_add3_u32 v0, v0, v32, s90
	ds_write_b16_d16_hi v164, v0 offset:128
	v_sub_f32_e32 v0, v48, v156
	v_mul_f32_e32 v0, v0, v157
	v_bfe_u32 v32, v0, 16, 1
	v_add3_u32 v0, v0, v32, s90
	ds_write_b16_d16_hi v164, v0 offset:192
	v_sub_f32_e32 v0, v96, v156
	v_mul_f32_e32 v0, v0, v157
	v_bfe_u32 v32, v0, 16, 1
	v_add3_u32 v0, v0, v32, s90
	ds_write_b16_d16_hi v164, v0 offset:256
	v_sub_f32_e32 v0, v112, v156
	v_mul_f32_e32 v0, v0, v157
	v_bfe_u32 v32, v0, 16, 1
	v_add3_u32 v0, v0, v32, s90
	ds_write_b16_d16_hi v164, v0 offset:320
	v_sub_f32_e32 v0, v80, v156
	v_mul_f32_e32 v0, v0, v157
	v_bfe_u32 v32, v0, 16, 1
	v_add3_u32 v0, v0, v32, s90
	ds_write_b16_d16_hi v164, v0 offset:384
	v_sub_f32_e32 v0, v64, v156
	v_mul_f32_e32 v0, v0, v157
	v_pk_add_f32 v[156:157], v[158:159], v[166:167]
	ds_write_b16_d16_hi v164, v172
	v_pk_mul_f32 v[156:157], v[156:157], s[36:37] op_sel_hi:[1,0]
	s_nop 0
	v_fma_f32 v32, -v156, v156, v157
	v_max_f32_e32 v32, 0, v32
	v_add_f32_e32 v32, 0x358637bd, v32
	v_mul_f32_e32 v48, 0x4b800000, v32
	v_cmp_gt_f32_e32 vcc, s89, v32
	v_sub_f32_e32 v17, v17, v156
	v_sub_f32_e32 v1, v1, v156
	v_cndmask_b32_e32 v32, v32, v48, vcc
	v_rsq_f32_e32 v32, v32
	v_bfe_u32 v48, v0, 16, 1
	v_add3_u32 v0, v0, v48, s90
	ds_write_b16_d16_hi v164, v0 offset:448
	v_mul_f32_e32 v0, 0x45800000, v32
	v_cndmask_b32_e32 v0, v32, v0, vcc
	v_mul_f32_e32 v17, v17, v0
	v_lshlrev_b32_e32 v32, 10, v218
	v_bfe_u32 v48, v17, 16, 1
	v_add3_u32 v17, v17, v48, s90
	v_add3_u32 v32, 0, v32, v16
	v_mul_f32_e32 v1, v1, v0
	ds_write_b16_d16_hi v32, v17
	v_bfe_u32 v17, v1, 16, 1
	v_add3_u32 v1, v1, v17, s90
	ds_write_b16_d16_hi v32, v1 offset:64
	v_sub_f32_e32 v1, v33, v156
	v_mul_f32_e32 v1, v1, v0
	v_bfe_u32 v17, v1, 16, 1
	v_add3_u32 v1, v1, v17, s90
	ds_write_b16_d16_hi v32, v1 offset:128
	v_sub_f32_e32 v1, v49, v156
	v_mul_f32_e32 v1, v1, v0
	v_bfe_u32 v17, v1, 16, 1
	v_add3_u32 v1, v1, v17, s90
	ds_write_b16_d16_hi v32, v1 offset:192
	v_sub_f32_e32 v1, v97, v156
	v_mul_f32_e32 v1, v1, v0
	v_bfe_u32 v17, v1, 16, 1
	v_add3_u32 v1, v1, v17, s90
	ds_write_b16_d16_hi v32, v1 offset:256
	v_sub_f32_e32 v1, v113, v156
	v_mul_f32_e32 v1, v1, v0
	v_bfe_u32 v17, v1, 16, 1
	v_add3_u32 v1, v1, v17, s90
	ds_write_b16_d16_hi v32, v1 offset:320
	v_sub_f32_e32 v1, v81, v156
	v_mul_f32_e32 v1, v1, v0
	v_bfe_u32 v17, v1, 16, 1
	v_add3_u32 v1, v1, v17, s90
	ds_write_b16_d16_hi v32, v1 offset:384
	v_sub_f32_e32 v1, v65, v156
	v_mul_f32_e32 v17, v1, v0
	s_waitcnt lgkmcnt(14)
	v_pk_add_f32 v[0:1], v[152:153], v[168:169]
	s_nop 0
	v_pk_mul_f32 v[0:1], v[0:1], s[36:37] op_sel_hi:[1,0]
	s_nop 0
	v_fma_f32 v1, -v0, v0, v1
	v_max_f32_e32 v1, 0, v1
	v_add_f32_e32 v1, 0x358637bd, v1
	v_mul_f32_e32 v33, 0x4b800000, v1
	v_cmp_gt_f32_e32 vcc, s89, v1
	v_sub_f32_e32 v18, v18, v0
	v_sub_f32_e32 v2, v2, v0
	v_cndmask_b32_e32 v1, v1, v33, vcc
	v_rsq_f32_e32 v1, v1
	v_bfe_u32 v33, v17, 16, 1
	v_add3_u32 v17, v17, v33, s90
	ds_write_b16_d16_hi v32, v17 offset:448
	v_mul_f32_e32 v17, 0x45800000, v1
	v_cndmask_b32_e32 v1, v1, v17, vcc
	v_mul_f32_e32 v18, v18, v1
	v_lshlrev_b32_e32 v17, 10, v217
	v_bfe_u32 v32, v18, 16, 1
	v_add3_u32 v18, v18, v32, s90
	v_add3_u32 v17, 0, v17, v16
	v_mul_f32_e32 v2, v2, v1
	ds_write_b16_d16_hi v17, v18
	v_bfe_u32 v18, v2, 16, 1
	v_add3_u32 v2, v2, v18, s90
	ds_write_b16_d16_hi v17, v2 offset:64
	v_sub_f32_e32 v2, v34, v0
	v_mul_f32_e32 v2, v2, v1
	v_bfe_u32 v18, v2, 16, 1
	v_add3_u32 v2, v2, v18, s90
	ds_write_b16_d16_hi v17, v2 offset:128
	v_sub_f32_e32 v2, v50, v0
	v_mul_f32_e32 v2, v2, v1
	v_bfe_u32 v18, v2, 16, 1
	v_add3_u32 v2, v2, v18, s90
	ds_write_b16_d16_hi v17, v2 offset:192
	v_sub_f32_e32 v2, v98, v0
	v_mul_f32_e32 v2, v2, v1
	v_bfe_u32 v18, v2, 16, 1
	v_add3_u32 v2, v2, v18, s90
	ds_write_b16_d16_hi v17, v2 offset:256
	v_sub_f32_e32 v2, v114, v0
	v_mul_f32_e32 v2, v2, v1
	v_bfe_u32 v18, v2, 16, 1
	v_add3_u32 v2, v2, v18, s90
	ds_write_b16_d16_hi v17, v2 offset:320
	v_sub_f32_e32 v2, v82, v0
	v_mul_f32_e32 v2, v2, v1
	v_bfe_u32 v18, v2, 16, 1
	v_add3_u32 v2, v2, v18, s90
	v_sub_f32_e32 v0, v66, v0
	ds_write_b16_d16_hi v17, v2 offset:384
	v_mul_f32_e32 v2, v0, v1
	v_pk_add_f32 v[0:1], v[154:155], v[170:171]
	s_nop 0
	v_pk_mul_f32 v[0:1], v[0:1], s[36:37] op_sel_hi:[1,0]
	s_nop 0
	v_fma_f32 v1, -v0, v0, v1
	v_max_f32_e32 v1, 0, v1
; #define LAS __attribute__((address_space(3)))
; __device__ __forceinline__ bf16_t f2bf(float f) { unsigned u = __builtin_bit_cast(unsigned, f); return (bf16_t)((u + 0x7fffu + ((u >> 16) & 1u)) >> 16); }
; __device__ __forceinline__ int crow(int r, int hi) { return (r & 3) + 8 * (r >> 2) + 4 * hi; }
; __device__ __forceinline__ int crow(int r, int hi) { return (r & 3) + 8 * (r >> 2) + 4 * hi; }
; template <int DK, int DV, bool MLSTM>
; __device__ __forceinline__ void out_unit2(LAS unsigned char* lds, LAS unsigned char* ldstab, const OutArgs a, const int wv) {
;     ...
;     for (int r = 0; r < 16; ++r) {
;         const int row = 32 * rb + crow(r, hi);
;         const float t1 = s1[r] + exch[((1 - dh) * 128 + row) * 2], t2 = s2[r] + exch[((1 - dh) * 128 + row) * 2 + 1];
;         float mean, inv;
;         if (MLSTM) { mean = 0.f; inv = rsqrtf(t2 * (1.f / DV) + EPS); }
;         else { mean = t1 * (1.f / DV); inv = rsqrtf(fmaxf(t2 * (1.f / DV) - mean * mean, 0.f) + EPS); }
; #pragma unroll
;         for (int nb = 0; nb < NB; ++nb) { const int col = dh * (DV / 2) + 32 * nb + r32;
;             *(LAS bf16_t*)(lds + row * TP + col * 2) = f2bf((o[nb][r] - mean) * inv); }
;     }
	v_add_f32_e32 v1, 0x358637bd, v1
	v_mul_f32_e32 v18, 0x4b800000, v1
	v_cmp_gt_f32_e32 vcc, s89, v1
	s_nop 1
	v_cndmask_b32_e32 v1, v1, v18, vcc
	v_rsq_f32_e32 v1, v1
	v_bfe_u32 v18, v2, 16, 1
	v_add3_u32 v2, v2, v18, s90
	ds_write_b16_d16_hi v17, v2 offset:448
	v_mul_f32_e32 v2, 0x45800000, v1
	v_cndmask_b32_e32 v1, v1, v2, vcc
	v_sub_f32_e32 v17, v19, v0
	v_mul_f32_e32 v17, v17, v1
	v_lshlrev_b32_e32 v2, 10, v216
	v_bfe_u32 v18, v17, 16, 1
	v_add3_u32 v17, v17, v18, s90
	v_add3_u32 v18, 0, v2, v16
	v_sub_f32_e32 v2, v3, v0
	v_mul_f32_e32 v2, v2, v1
	v_bfe_u32 v3, v2, 16, 1
	v_add3_u32 v2, v2, v3, s90
	ds_write_b16_d16_hi v18, v2 offset:64
	v_sub_f32_e32 v2, v35, v0
	v_mul_f32_e32 v2, v2, v1
	v_bfe_u32 v3, v2, 16, 1
	v_add3_u32 v2, v2, v3, s90
	ds_write_b16_d16_hi v18, v2 offset:128
	v_sub_f32_e32 v2, v51, v0
	v_mul_f32_e32 v2, v2, v1
	v_bfe_u32 v3, v2, 16, 1
	v_add3_u32 v2, v2, v3, s90
	ds_write_b16_d16_hi v18, v2 offset:192
	v_sub_f32_e32 v2, v99, v0
	v_mul_f32_e32 v2, v2, v1
	v_bfe_u32 v3, v2, 16, 1
	v_add3_u32 v2, v2, v3, s90
	ds_write_b16_d16_hi v18, v2 offset:256
	v_sub_f32_e32 v2, v115, v0
	v_mul_f32_e32 v2, v2, v1
	v_bfe_u32 v3, v2, 16, 1
	v_add3_u32 v2, v2, v3, s90
	ds_write_b16_d16_hi v18, v2 offset:320
	v_sub_f32_e32 v2, v83, v0
	v_sub_f32_e32 v0, v67, v0
	ds_write_b16_d16_hi v18, v17
	v_mul_f32_e32 v2, v2, v1
	v_mul_f32_e32 v17, v0, v1
	v_lshlrev_b32_e32 v0, 1, v215
	v_bfe_u32 v3, v2, 16, 1
	v_subrev_u32_e32 v0, s6, v0
	v_add3_u32 v2, v2, v3, s90
	v_lshl_add_u32 v0, v0, 2, s4
	ds_write_b16_d16_hi v18, v2 offset:384
	ds_read2_b64 v[0:3], v0 offset0:128 offset1:129
	v_lshlrev_b32_e32 v19, 1, v213
	v_subrev_u32_e32 v19, s6, v19
	v_lshl_add_u32 v19, v19, 2, s4
	ds_read2_b64 v[32:35], v19 offset0:128 offset1:129
	s_waitcnt lgkmcnt(1)
	v_pk_add_f32 v[0:1], v[148:149], v[0:1]
	s_nop 0
	v_pk_mul_f32 v[0:1], v[0:1], s[36:37] op_sel_hi:[1,0]
	s_nop 0
	v_fma_f32 v1, -v0, v0, v1
	v_max_f32_e32 v1, 0, v1
	v_add_f32_e32 v1, 0x358637bd, v1
	v_mul_f32_e32 v19, 0x4b800000, v1
	v_cmp_gt_f32_e32 vcc, s89, v1
	v_sub_f32_e32 v4, v4, v0
	s_nop 0
	v_cndmask_b32_e32 v1, v1, v19, vcc
	v_rsq_f32_e32 v1, v1
	v_bfe_u32 v19, v17, 16, 1
	v_add3_u32 v17, v17, v19, s90
	ds_write_b16_d16_hi v18, v17 offset:448
	v_mul_f32_e32 v17, 0x45800000, v1
	v_cndmask_b32_e32 v1, v1, v17, vcc
	v_sub_f32_e32 v18, v20, v0
	v_mul_f32_e32 v18, v18, v1
	v_lshlrev_b32_e32 v17, 10, v215
	v_bfe_u32 v19, v18, 16, 1
	v_add3_u32 v18, v18, v19, s90
	v_add3_u32 v17, 0, v17, v16
	v_mul_f32_e32 v4, v4, v1
	ds_write_b16_d16_hi v17, v18
	v_bfe_u32 v18, v4, 16, 1
	v_add3_u32 v4, v4, v18, s90
	ds_write_b16_d16_hi v17, v4 offset:64
	v_sub_f32_e32 v4, v36, v0
	v_mul_f32_e32 v4, v4, v1
	v_bfe_u32 v18, v4, 16, 1
	v_add3_u32 v4, v4, v18, s90
	ds_write_b16_d16_hi v17, v4 offset:128
	v_sub_f32_e32 v4, v52, v0
	v_mul_f32_e32 v4, v4, v1
	v_bfe_u32 v18, v4, 16, 1
	v_add3_u32 v4, v4, v18, s90
	ds_write_b16_d16_hi v17, v4 offset:192
	v_sub_f32_e32 v4, v100, v0
	v_mul_f32_e32 v4, v4, v1
	v_bfe_u32 v18, v4, 16, 1
	v_add3_u32 v4, v4, v18, s90
	ds_write_b16_d16_hi v17, v4 offset:256
	v_sub_f32_e32 v4, v116, v0
	v_mul_f32_e32 v4, v4, v1
	v_bfe_u32 v18, v4, 16, 1
	v_add3_u32 v4, v4, v18, s90
	ds_write_b16_d16_hi v17, v4 offset:320
	v_sub_f32_e32 v4, v84, v0
	v_mul_f32_e32 v4, v4, v1
	v_bfe_u32 v18, v4, 16, 1
	v_add3_u32 v4, v4, v18, s90
	v_sub_f32_e32 v0, v68, v0
	ds_write_b16_d16_hi v17, v4 offset:384
	v_mul_f32_e32 v4, v0, v1
	v_pk_add_f32 v[0:1], v[150:151], v[2:3]
	s_nop 0
	v_pk_mul_f32 v[0:1], v[0:1], s[36:37] op_sel_hi:[1,0]
	s_nop 0
	v_fma_f32 v1, -v0, v0, v1
	v_max_f32_e32 v1, 0, v1
	v_add_f32_e32 v1, 0x358637bd, v1
	v_mul_f32_e32 v2, 0x4b800000, v1
	v_cmp_gt_f32_e32 vcc, s89, v1
	v_sub_f32_e32 v3, v21, v0
	s_nop 0
	v_cndmask_b32_e32 v1, v1, v2, vcc
	v_rsq_f32_e32 v1, v1
	v_bfe_u32 v2, v4, 16, 1
	v_add3_u32 v2, v4, v2, s90
	ds_write_b16_d16_hi v17, v2 offset:448
	v_mul_f32_e32 v2, 0x45800000, v1
	v_cndmask_b32_e32 v1, v1, v2, vcc
	v_mul_f32_e32 v3, v3, v1
	v_lshlrev_b32_e32 v2, 10, v214
	v_bfe_u32 v4, v3, 16, 1
	v_add3_u32 v3, v3, v4, s90
	v_add3_u32 v2, 0, v2, v16
	ds_write_b16_d16_hi v2, v3
	v_sub_f32_e32 v3, v5, v0
	v_mul_f32_e32 v3, v3, v1
	v_bfe_u32 v4, v3, 16, 1
	v_add3_u32 v3, v3, v4, s90
	ds_write_b16_d16_hi v2, v3 offset:64
	v_sub_f32_e32 v3, v37, v0
	v_mul_f32_e32 v3, v3, v1
	v_bfe_u32 v4, v3, 16, 1
	v_add3_u32 v3, v3, v4, s90
	ds_write_b16_d16_hi v2, v3 offset:128
	v_sub_f32_e32 v3, v53, v0
	v_mul_f32_e32 v3, v3, v1
	v_bfe_u32 v4, v3, 16, 1
	v_add3_u32 v3, v3, v4, s90
	ds_write_b16_d16_hi v2, v3 offset:192
	v_sub_f32_e32 v3, v101, v0
	v_mul_f32_e32 v3, v3, v1
	v_bfe_u32 v4, v3, 16, 1
	v_add3_u32 v3, v3, v4, s90
	ds_write_b16_d16_hi v2, v3 offset:256
	v_sub_f32_e32 v3, v117, v0
	v_mul_f32_e32 v3, v3, v1
	v_bfe_u32 v4, v3, 16, 1
	v_add3_u32 v3, v3, v4, s90
	ds_write_b16_d16_hi v2, v3 offset:320
	v_sub_f32_e32 v3, v85, v0
	v_mul_f32_e32 v3, v3, v1
	v_bfe_u32 v4, v3, 16, 1
	v_add3_u32 v3, v3, v4, s90
	v_sub_f32_e32 v0, v69, v0
	ds_write_b16_d16_hi v2, v3 offset:384
	v_mul_f32_e32 v3, v0, v1
	s_waitcnt lgkmcnt(14)
; #define LAS __attribute__((address_space(3)))
; __device__ __forceinline__ bf16_t f2bf(float f) { unsigned u = __builtin_bit_cast(unsigned, f); return (bf16_t)((u + 0x7fffu + ((u >> 16) & 1u)) >> 16); }
; __device__ __forceinline__ int crow(int r, int hi) { return (r & 3) + 8 * (r >> 2) + 4 * hi; }
; __device__ __forceinline__ int crow(int r, int hi) { return (r & 3) + 8 * (r >> 2) + 4 * hi; }
; template <int DK, int DV, bool MLSTM>
; __device__ __forceinline__ void out_unit2(LAS unsigned char* lds, LAS unsigned char* ldstab, const OutArgs a, const int wv) {
;     ...
;     for (int r = 0; r < 16; ++r) {
;         const int row = 32 * rb + crow(r, hi);
;         const float t1 = s1[r] + exch[((1 - dh) * 128 + row) * 2], t2 = s2[r] + exch[((1 - dh) * 128 + row) * 2 + 1];
;         float mean, inv;
;         if (MLSTM) { mean = 0.f; inv = rsqrtf(t2 * (1.f / DV) + EPS); }
;         else { mean = t1 * (1.f / DV); inv = rsqrtf(fmaxf(t2 * (1.f / DV) - mean * mean, 0.f) + EPS); }
; #pragma unroll
;         for (int nb = 0; nb < NB; ++nb) { const int col = dh * (DV / 2) + 32 * nb + r32;
;             *(LAS bf16_t*)(lds + row * TP + col * 2) = f2bf((o[nb][r] - mean) * inv); }
;     }
	v_pk_add_f32 v[0:1], v[144:145], v[32:33]
	s_nop 0
	v_pk_mul_f32 v[0:1], v[0:1], s[36:37] op_sel_hi:[1,0]
	s_nop 0
	v_fma_f32 v1, -v0, v0, v1
	v_max_f32_e32 v1, 0, v1
	v_add_f32_e32 v1, 0x358637bd, v1
	v_mul_f32_e32 v4, 0x4b800000, v1
	v_cmp_gt_f32_e32 vcc, s89, v1
	s_nop 1
	v_cndmask_b32_e32 v1, v1, v4, vcc
	v_rsq_f32_e32 v1, v1
	v_bfe_u32 v4, v3, 16, 1
	v_add3_u32 v3, v3, v4, s90
	ds_write_b16_d16_hi v2, v3 offset:448
	v_mul_f32_e32 v2, 0x45800000, v1
	v_cndmask_b32_e32 v1, v1, v2, vcc
	v_sub_f32_e32 v3, v22, v0
	v_mul_f32_e32 v3, v3, v1
	v_lshlrev_b32_e32 v2, 10, v213
	v_bfe_u32 v4, v3, 16, 1
	v_add3_u32 v3, v3, v4, s90
	v_add3_u32 v2, 0, v2, v16
	ds_write_b16_d16_hi v2, v3
	v_sub_f32_e32 v3, v6, v0
	v_mul_f32_e32 v3, v3, v1
	v_bfe_u32 v4, v3, 16, 1
	v_add3_u32 v3, v3, v4, s90
	ds_write_b16_d16_hi v2, v3 offset:64
	v_sub_f32_e32 v3, v38, v0
	v_mul_f32_e32 v3, v3, v1
	v_bfe_u32 v4, v3, 16, 1
	v_add3_u32 v3, v3, v4, s90
	ds_write_b16_d16_hi v2, v3 offset:128
	v_sub_f32_e32 v3, v54, v0
	v_mul_f32_e32 v3, v3, v1
	v_bfe_u32 v4, v3, 16, 1
	v_add3_u32 v3, v3, v4, s90
	ds_write_b16_d16_hi v2, v3 offset:192
	v_sub_f32_e32 v3, v102, v0
	v_mul_f32_e32 v3, v3, v1
	v_bfe_u32 v4, v3, 16, 1
	v_add3_u32 v3, v3, v4, s90
	ds_write_b16_d16_hi v2, v3 offset:256
	v_sub_f32_e32 v3, v118, v0
	v_mul_f32_e32 v3, v3, v1
	v_bfe_u32 v4, v3, 16, 1
	v_add3_u32 v3, v3, v4, s90
	ds_write_b16_d16_hi v2, v3 offset:320
	v_sub_f32_e32 v3, v86, v0
	v_mul_f32_e32 v3, v3, v1
	v_bfe_u32 v4, v3, 16, 1
	v_add3_u32 v3, v3, v4, s90
	v_sub_f32_e32 v0, v70, v0
	ds_write_b16_d16_hi v2, v3 offset:384
	v_mul_f32_e32 v3, v0, v1
	v_pk_add_f32 v[0:1], v[146:147], v[34:35]
	s_nop 0
	v_pk_mul_f32 v[0:1], v[0:1], s[36:37] op_sel_hi:[1,0]
	s_nop 0
	v_fma_f32 v1, -v0, v0, v1
	v_max_f32_e32 v1, 0, v1
	v_add_f32_e32 v1, 0x358637bd, v1
	v_mul_f32_e32 v4, 0x4b800000, v1
	v_cmp_gt_f32_e32 vcc, s89, v1
	s_nop 1
	v_cndmask_b32_e32 v1, v1, v4, vcc
	v_rsq_f32_e32 v1, v1
	v_bfe_u32 v4, v3, 16, 1
	v_add3_u32 v3, v3, v4, s90
	ds_write_b16_d16_hi v2, v3 offset:448
	v_mul_f32_e32 v2, 0x45800000, v1
	v_cndmask_b32_e32 v1, v1, v2, vcc
	v_sub_f32_e32 v3, v23, v0
	v_lshlrev_b32_e32 v2, 10, v212
	v_mul_f32_e32 v3, v3, v1
	v_bfe_u32 v4, v3, 16, 1
	v_add3_u32 v17, 0, v2, v16
	v_sub_f32_e32 v2, v7, v0
	v_add3_u32 v3, v3, v4, s90
	v_mul_f32_e32 v2, v2, v1
	ds_write_b16_d16_hi v17, v3
	v_bfe_u32 v3, v2, 16, 1
	v_add3_u32 v2, v2, v3, s90
	ds_write_b16_d16_hi v17, v2 offset:64
	v_sub_f32_e32 v2, v39, v0
	v_mul_f32_e32 v2, v2, v1
	v_bfe_u32 v3, v2, 16, 1
	v_add3_u32 v2, v2, v3, s90
	ds_write_b16_d16_hi v17, v2 offset:128
	v_sub_f32_e32 v2, v55, v0
	v_mul_f32_e32 v2, v2, v1
	v_bfe_u32 v3, v2, 16, 1
	v_add3_u32 v2, v2, v3, s90
	ds_write_b16_d16_hi v17, v2 offset:192
	v_sub_f32_e32 v2, v103, v0
	v_mul_f32_e32 v2, v2, v1
	v_bfe_u32 v3, v2, 16, 1
	v_add3_u32 v2, v2, v3, s90
	ds_write_b16_d16_hi v17, v2 offset:256
	v_sub_f32_e32 v2, v119, v0
	v_mul_f32_e32 v2, v2, v1
	v_bfe_u32 v3, v2, 16, 1
	v_add3_u32 v2, v2, v3, s90
	ds_write_b16_d16_hi v17, v2 offset:320
	v_sub_f32_e32 v2, v87, v0
	v_sub_f32_e32 v0, v71, v0
	v_mul_f32_e32 v2, v2, v1
	v_mul_f32_e32 v18, v0, v1
	v_lshlrev_b32_e32 v0, 1, v211
	v_bfe_u32 v3, v2, 16, 1
	v_subrev_u32_e32 v0, s6, v0
	v_add3_u32 v2, v2, v3, s90
	v_lshl_add_u32 v0, v0, 2, s4
	ds_write_b16_d16_hi v17, v2 offset:384
	ds_read2_b64 v[0:3], v0 offset0:128 offset1:129
	v_lshlrev_b32_e32 v4, 1, v209
	v_subrev_u32_e32 v4, s6, v4
	v_lshl_add_u32 v4, v4, 2, s4
	ds_read2_b64 v[4:7], v4 offset0:128 offset1:129
	s_waitcnt lgkmcnt(1)
	v_pk_add_f32 v[0:1], v[140:141], v[0:1]
	s_nop 0
	v_pk_mul_f32 v[0:1], v[0:1], s[36:37] op_sel_hi:[1,0]
	s_nop 0
	v_fma_f32 v1, -v0, v0, v1
	v_max_f32_e32 v1, 0, v1
	v_add_f32_e32 v1, 0x358637bd, v1
	v_mul_f32_e32 v19, 0x4b800000, v1
	v_cmp_gt_f32_e32 vcc, s89, v1
	v_sub_f32_e32 v8, v8, v0
	s_nop 0
	v_cndmask_b32_e32 v1, v1, v19, vcc
	v_rsq_f32_e32 v1, v1
	v_bfe_u32 v19, v18, 16, 1
	v_add3_u32 v18, v18, v19, s90
	ds_write_b16_d16_hi v17, v18 offset:448
	v_mul_f32_e32 v17, 0x45800000, v1
	v_cndmask_b32_e32 v1, v1, v17, vcc
	v_sub_f32_e32 v18, v24, v0
	v_mul_f32_e32 v18, v18, v1
	v_lshlrev_b32_e32 v17, 10, v211
	v_bfe_u32 v19, v18, 16, 1
	v_add3_u32 v18, v18, v19, s90
	v_add3_u32 v17, 0, v17, v16
	v_mul_f32_e32 v8, v8, v1
	ds_write_b16_d16_hi v17, v18
	v_bfe_u32 v18, v8, 16, 1
	v_add3_u32 v8, v8, v18, s90
	ds_write_b16_d16_hi v17, v8 offset:64
	v_sub_f32_e32 v8, v40, v0
	v_mul_f32_e32 v8, v8, v1
	v_bfe_u32 v18, v8, 16, 1
	v_add3_u32 v8, v8, v18, s90
	ds_write_b16_d16_hi v17, v8 offset:128
	v_sub_f32_e32 v8, v56, v0
	v_mul_f32_e32 v8, v8, v1
	v_bfe_u32 v18, v8, 16, 1
	v_add3_u32 v8, v8, v18, s90
	ds_write_b16_d16_hi v17, v8 offset:192
	v_sub_f32_e32 v8, v104, v0
	v_mul_f32_e32 v8, v8, v1
	v_bfe_u32 v18, v8, 16, 1
	v_add3_u32 v8, v8, v18, s90
	ds_write_b16_d16_hi v17, v8 offset:256
	v_sub_f32_e32 v8, v120, v0
	v_mul_f32_e32 v8, v8, v1
	v_bfe_u32 v18, v8, 16, 1
	v_add3_u32 v8, v8, v18, s90
	ds_write_b16_d16_hi v17, v8 offset:320
	v_sub_f32_e32 v8, v88, v0
	v_mul_f32_e32 v8, v8, v1
	v_bfe_u32 v18, v8, 16, 1
	v_add3_u32 v8, v8, v18, s90
	v_sub_f32_e32 v0, v72, v0
	ds_write_b16_d16_hi v17, v8 offset:384
	v_mul_f32_e32 v8, v0, v1
	v_pk_add_f32 v[0:1], v[142:143], v[2:3]
	s_nop 0
	v_pk_mul_f32 v[0:1], v[0:1], s[36:37] op_sel_hi:[1,0]
	s_nop 0
	v_fma_f32 v1, -v0, v0, v1
	v_max_f32_e32 v1, 0, v1
	v_add_f32_e32 v1, 0x358637bd, v1
	v_mul_f32_e32 v2, 0x4b800000, v1
	v_cmp_gt_f32_e32 vcc, s89, v1
	v_sub_f32_e32 v3, v25, v0
	s_nop 0
	v_cndmask_b32_e32 v1, v1, v2, vcc
	v_rsq_f32_e32 v1, v1
	v_bfe_u32 v2, v8, 16, 1
	v_add3_u32 v2, v8, v2, s90
	ds_write_b16_d16_hi v17, v2 offset:448
	v_mul_f32_e32 v2, 0x45800000, v1
	v_cndmask_b32_e32 v1, v1, v2, vcc
	v_mul_f32_e32 v3, v3, v1
	v_lshlrev_b32_e32 v2, 10, v210
	v_bfe_u32 v8, v3, 16, 1
	v_add3_u32 v3, v3, v8, s90
	v_add3_u32 v2, 0, v2, v16
	ds_write_b16_d16_hi v2, v3
	v_sub_f32_e32 v3, v9, v0
	v_mul_f32_e32 v3, v3, v1
	v_bfe_u32 v8, v3, 16, 1
	v_add3_u32 v3, v3, v8, s90
	ds_write_b16_d16_hi v2, v3 offset:64
	v_sub_f32_e32 v3, v41, v0
	v_mul_f32_e32 v3, v3, v1
	v_bfe_u32 v8, v3, 16, 1
	v_add3_u32 v3, v3, v8, s90
	ds_write_b16_d16_hi v2, v3 offset:128
	v_sub_f32_e32 v3, v57, v0
	v_mul_f32_e32 v3, v3, v1
	v_bfe_u32 v8, v3, 16, 1
	v_add3_u32 v3, v3, v8, s90
	ds_write_b16_d16_hi v2, v3 offset:192
	v_sub_f32_e32 v3, v105, v0
	v_mul_f32_e32 v3, v3, v1
	v_bfe_u32 v8, v3, 16, 1
	v_add3_u32 v3, v3, v8, s90
	ds_write_b16_d16_hi v2, v3 offset:256
	v_sub_f32_e32 v3, v121, v0
	v_mul_f32_e32 v3, v3, v1
	v_bfe_u32 v8, v3, 16, 1
	v_add3_u32 v3, v3, v8, s90
	ds_write_b16_d16_hi v2, v3 offset:320
	v_sub_f32_e32 v3, v89, v0
	v_mul_f32_e32 v3, v3, v1
	v_bfe_u32 v8, v3, 16, 1
	v_add3_u32 v3, v3, v8, s90
	v_sub_f32_e32 v0, v73, v0
	ds_write_b16_d16_hi v2, v3 offset:384
	v_mul_f32_e32 v3, v0, v1
	s_waitcnt lgkmcnt(14)
; #define LAS __attribute__((address_space(3)))
; __device__ __forceinline__ bf16_t f2bf(float f) { unsigned u = __builtin_bit_cast(unsigned, f); return (bf16_t)((u + 0x7fffu + ((u >> 16) & 1u)) >> 16); }
; __device__ __forceinline__ int crow(int r, int hi) { return (r & 3) + 8 * (r >> 2) + 4 * hi; }
; __device__ __forceinline__ int crow(int r, int hi) { return (r & 3) + 8 * (r >> 2) + 4 * hi; }
; template <int DK, int DV, bool MLSTM>
; __device__ __forceinline__ void out_unit2(LAS unsigned char* lds, LAS unsigned char* ldstab, const OutArgs a, const int wv) {
;     ...
;     for (int r = 0; r < 16; ++r) {
;         const int row = 32 * rb + crow(r, hi);
;         const float t1 = s1[r] + exch[((1 - dh) * 128 + row) * 2], t2 = s2[r] + exch[((1 - dh) * 128 + row) * 2 + 1];
;         float mean, inv;
;         if (MLSTM) { mean = 0.f; inv = rsqrtf(t2 * (1.f / DV) + EPS); }
;         else { mean = t1 * (1.f / DV); inv = rsqrtf(fmaxf(t2 * (1.f / DV) - mean * mean, 0.f) + EPS); }
; #pragma unroll
;         for (int nb = 0; nb < NB; ++nb) { const int col = dh * (DV / 2) + 32 * nb + r32;
;             *(LAS bf16_t*)(lds + row * TP + col * 2) = f2bf((o[nb][r] - mean) * inv); }
;     }
	v_pk_add_f32 v[0:1], v[136:137], v[4:5]
	s_nop 0
	v_pk_mul_f32 v[0:1], v[0:1], s[36:37] op_sel_hi:[1,0]
	s_nop 0
	v_fma_f32 v1, -v0, v0, v1
	v_max_f32_e32 v1, 0, v1
	v_add_f32_e32 v1, 0x358637bd, v1
	v_mul_f32_e32 v4, 0x4b800000, v1
	v_cmp_gt_f32_e32 vcc, s89, v1
	s_nop 1
	v_cndmask_b32_e32 v1, v1, v4, vcc
	v_rsq_f32_e32 v1, v1
	v_bfe_u32 v4, v3, 16, 1
	v_add3_u32 v3, v3, v4, s90
	ds_write_b16_d16_hi v2, v3 offset:448
	v_mul_f32_e32 v2, 0x45800000, v1
	v_cndmask_b32_e32 v1, v1, v2, vcc
	v_sub_f32_e32 v3, v26, v0
	v_mul_f32_e32 v3, v3, v1
	v_lshlrev_b32_e32 v2, 10, v209
	v_bfe_u32 v4, v3, 16, 1
	v_add3_u32 v3, v3, v4, s90
	v_add3_u32 v2, 0, v2, v16
	ds_write_b16_d16_hi v2, v3
	v_sub_f32_e32 v3, v10, v0
	v_mul_f32_e32 v3, v3, v1
	v_bfe_u32 v4, v3, 16, 1
	v_add3_u32 v3, v3, v4, s90
	ds_write_b16_d16_hi v2, v3 offset:64
	v_sub_f32_e32 v3, v42, v0
	v_mul_f32_e32 v3, v3, v1
	v_bfe_u32 v4, v3, 16, 1
	v_add3_u32 v3, v3, v4, s90
	ds_write_b16_d16_hi v2, v3 offset:128
	v_sub_f32_e32 v3, v58, v0
	v_mul_f32_e32 v3, v3, v1
	v_bfe_u32 v4, v3, 16, 1
	v_add3_u32 v3, v3, v4, s90
	ds_write_b16_d16_hi v2, v3 offset:192
	v_sub_f32_e32 v3, v106, v0
	v_mul_f32_e32 v3, v3, v1
	v_bfe_u32 v4, v3, 16, 1
	v_add3_u32 v3, v3, v4, s90
	ds_write_b16_d16_hi v2, v3 offset:256
	v_sub_f32_e32 v3, v122, v0
	v_mul_f32_e32 v3, v3, v1
	v_bfe_u32 v4, v3, 16, 1
	v_add3_u32 v3, v3, v4, s90
	ds_write_b16_d16_hi v2, v3 offset:320
	v_sub_f32_e32 v3, v90, v0
	v_mul_f32_e32 v3, v3, v1
	v_bfe_u32 v4, v3, 16, 1
	v_add3_u32 v3, v3, v4, s90
	v_sub_f32_e32 v0, v74, v0
	ds_write_b16_d16_hi v2, v3 offset:384
	v_mul_f32_e32 v3, v0, v1
	v_pk_add_f32 v[0:1], v[138:139], v[6:7]
	s_nop 0
	v_pk_mul_f32 v[0:1], v[0:1], s[36:37] op_sel_hi:[1,0]
	s_nop 0
	v_fma_f32 v1, -v0, v0, v1
	v_max_f32_e32 v1, 0, v1
	v_add_f32_e32 v1, 0x358637bd, v1
	v_mul_f32_e32 v4, 0x4b800000, v1
	v_cmp_gt_f32_e32 vcc, s89, v1
	s_nop 1
	v_cndmask_b32_e32 v1, v1, v4, vcc
	v_rsq_f32_e32 v1, v1
	v_bfe_u32 v4, v3, 16, 1
	v_add3_u32 v3, v3, v4, s90
	ds_write_b16_d16_hi v2, v3 offset:448
	v_mul_f32_e32 v2, 0x45800000, v1
	v_cndmask_b32_e32 v1, v1, v2, vcc
	v_sub_f32_e32 v3, v27, v0
	v_lshlrev_b32_e32 v2, 10, v208
	v_mul_f32_e32 v3, v3, v1
	v_bfe_u32 v4, v3, 16, 1
	v_add3_u32 v8, 0, v2, v16
	v_sub_f32_e32 v2, v11, v0
	v_add3_u32 v3, v3, v4, s90
	v_mul_f32_e32 v2, v2, v1
	ds_write_b16_d16_hi v8, v3
	v_bfe_u32 v3, v2, 16, 1
	v_add3_u32 v2, v2, v3, s90
	ds_write_b16_d16_hi v8, v2 offset:64
	v_sub_f32_e32 v2, v43, v0
	v_mul_f32_e32 v2, v2, v1
	v_bfe_u32 v3, v2, 16, 1
	v_add3_u32 v2, v2, v3, s90
	ds_write_b16_d16_hi v8, v2 offset:128
	v_sub_f32_e32 v2, v59, v0
	v_mul_f32_e32 v2, v2, v1
	v_bfe_u32 v3, v2, 16, 1
	v_add3_u32 v2, v2, v3, s90
	ds_write_b16_d16_hi v8, v2 offset:192
	v_sub_f32_e32 v2, v107, v0
	v_mul_f32_e32 v2, v2, v1
	v_bfe_u32 v3, v2, 16, 1
	v_add3_u32 v2, v2, v3, s90
	ds_write_b16_d16_hi v8, v2 offset:256
	v_sub_f32_e32 v2, v123, v0
	v_mul_f32_e32 v2, v2, v1
	v_bfe_u32 v3, v2, 16, 1
	v_add3_u32 v2, v2, v3, s90
	ds_write_b16_d16_hi v8, v2 offset:320
	v_sub_f32_e32 v2, v91, v0
	v_sub_f32_e32 v0, v75, v0
	v_mul_f32_e32 v2, v2, v1
	v_mul_f32_e32 v9, v0, v1
	v_lshlrev_b32_e32 v0, 1, v207
	v_bfe_u32 v3, v2, 16, 1
	v_subrev_u32_e32 v0, s6, v0
	v_add3_u32 v2, v2, v3, s90
	v_lshl_add_u32 v0, v0, 2, s4
	ds_write_b16_d16_hi v8, v2 offset:384
	ds_read2_b64 v[0:3], v0 offset0:128 offset1:129
	v_lshlrev_b32_e32 v4, 1, v162
	v_subrev_u32_e32 v4, s6, v4
	v_lshl_add_u32 v4, v4, 2, s4
	ds_read2_b64 v[4:7], v4 offset0:128 offset1:129
	s_waitcnt lgkmcnt(1)
	v_pk_add_f32 v[0:1], v[132:133], v[0:1]
	s_nop 0
	v_pk_mul_f32 v[0:1], v[0:1], s[36:37] op_sel_hi:[1,0]
	s_nop 0
	v_fma_f32 v1, -v0, v0, v1
	v_max_f32_e32 v1, 0, v1
	v_add_f32_e32 v1, 0x358637bd, v1
	v_mul_f32_e32 v10, 0x4b800000, v1
	v_cmp_gt_f32_e32 vcc, s89, v1
	s_nop 1
	v_cndmask_b32_e32 v1, v1, v10, vcc
	v_rsq_f32_e32 v1, v1
	v_bfe_u32 v10, v9, 16, 1
	v_add3_u32 v9, v9, v10, s90
	ds_write_b16_d16_hi v8, v9 offset:448
	v_mul_f32_e32 v8, 0x45800000, v1
	v_cndmask_b32_e32 v1, v1, v8, vcc
	v_sub_f32_e32 v9, v28, v0
	v_mul_f32_e32 v9, v9, v1
	v_lshlrev_b32_e32 v8, 10, v207
	v_bfe_u32 v10, v9, 16, 1
	v_add3_u32 v9, v9, v10, s90
	v_add3_u32 v8, 0, v8, v16
	ds_write_b16_d16_hi v8, v9
	v_sub_f32_e32 v9, v12, v0
	v_mul_f32_e32 v9, v9, v1
	v_bfe_u32 v10, v9, 16, 1
	v_add3_u32 v9, v9, v10, s90
	ds_write_b16_d16_hi v8, v9 offset:64
	v_sub_f32_e32 v9, v44, v0
	v_mul_f32_e32 v9, v9, v1
	v_bfe_u32 v10, v9, 16, 1
	v_add3_u32 v9, v9, v10, s90
	ds_write_b16_d16_hi v8, v9 offset:128
	v_sub_f32_e32 v9, v60, v0
	v_mul_f32_e32 v9, v9, v1
	v_bfe_u32 v10, v9, 16, 1
	v_add3_u32 v9, v9, v10, s90
	ds_write_b16_d16_hi v8, v9 offset:192
	v_sub_f32_e32 v9, v108, v0
	v_mul_f32_e32 v9, v9, v1
	v_bfe_u32 v10, v9, 16, 1
	v_add3_u32 v9, v9, v10, s90
	ds_write_b16_d16_hi v8, v9 offset:256
	v_sub_f32_e32 v9, v124, v0
	v_mul_f32_e32 v9, v9, v1
	v_bfe_u32 v10, v9, 16, 1
	v_add3_u32 v9, v9, v10, s90
	ds_write_b16_d16_hi v8, v9 offset:320
	v_sub_f32_e32 v9, v92, v0
	v_mul_f32_e32 v9, v9, v1
	v_bfe_u32 v10, v9, 16, 1
	v_add3_u32 v9, v9, v10, s90
	v_sub_f32_e32 v0, v76, v0
	ds_write_b16_d16_hi v8, v9 offset:384
	v_mul_f32_e32 v9, v0, v1
	v_pk_add_f32 v[0:1], v[134:135], v[2:3]
	s_nop 0
	v_pk_mul_f32 v[0:1], v[0:1], s[36:37] op_sel_hi:[1,0]
	s_nop 0
	v_fma_f32 v1, -v0, v0, v1
	v_max_f32_e32 v1, 0, v1
	v_add_f32_e32 v1, 0x358637bd, v1
	v_mul_f32_e32 v2, 0x4b800000, v1
	v_cmp_gt_f32_e32 vcc, s89, v1
	v_sub_f32_e32 v3, v29, v0
	s_nop 0
	v_cndmask_b32_e32 v1, v1, v2, vcc
	v_rsq_f32_e32 v1, v1
	v_bfe_u32 v2, v9, 16, 1
	v_add3_u32 v2, v9, v2, s90
	ds_write_b16_d16_hi v8, v2 offset:448
	v_mul_f32_e32 v2, 0x45800000, v1
	v_cndmask_b32_e32 v1, v1, v2, vcc
	v_mul_f32_e32 v3, v3, v1
	v_lshlrev_b32_e32 v2, 10, v206
	v_bfe_u32 v8, v3, 16, 1
	v_add3_u32 v3, v3, v8, s90
	v_add3_u32 v2, 0, v2, v16
	ds_write_b16_d16_hi v2, v3
	v_sub_f32_e32 v3, v13, v0
	v_mul_f32_e32 v3, v3, v1
	v_bfe_u32 v8, v3, 16, 1
	v_add3_u32 v3, v3, v8, s90
	ds_write_b16_d16_hi v2, v3 offset:64
	v_sub_f32_e32 v3, v45, v0
	v_mul_f32_e32 v3, v3, v1
	v_bfe_u32 v8, v3, 16, 1
	v_add3_u32 v3, v3, v8, s90
	ds_write_b16_d16_hi v2, v3 offset:128
	v_sub_f32_e32 v3, v61, v0
	v_mul_f32_e32 v3, v3, v1
	v_bfe_u32 v8, v3, 16, 1
	v_add3_u32 v3, v3, v8, s90
	ds_write_b16_d16_hi v2, v3 offset:192
	v_sub_f32_e32 v3, v109, v0
	v_mul_f32_e32 v3, v3, v1
	v_bfe_u32 v8, v3, 16, 1
	v_add3_u32 v3, v3, v8, s90
	ds_write_b16_d16_hi v2, v3 offset:256
	v_sub_f32_e32 v3, v125, v0
	v_mul_f32_e32 v3, v3, v1
	v_bfe_u32 v8, v3, 16, 1
	v_add3_u32 v3, v3, v8, s90
	ds_write_b16_d16_hi v2, v3 offset:320
	v_sub_f32_e32 v3, v93, v0
	v_mul_f32_e32 v3, v3, v1
	v_bfe_u32 v8, v3, 16, 1
	v_add3_u32 v3, v3, v8, s90
	v_sub_f32_e32 v0, v77, v0
	ds_write_b16_d16_hi v2, v3 offset:384
	v_mul_f32_e32 v3, v0, v1
	s_waitcnt lgkmcnt(14)
; #define LAS __attribute__((address_space(3)))
; __device__ __forceinline__ bf16_t f2bf(float f) { unsigned u = __builtin_bit_cast(unsigned, f); return (bf16_t)((u + 0x7fffu + ((u >> 16) & 1u)) >> 16); }
; __device__ __forceinline__ int crow(int r, int hi) { return (r & 3) + 8 * (r >> 2) + 4 * hi; }
; __device__ __forceinline__ int crow(int r, int hi) { return (r & 3) + 8 * (r >> 2) + 4 * hi; }
; template <int DK, int DV, bool MLSTM>
; __device__ __forceinline__ void out_unit2(LAS unsigned char* lds, LAS unsigned char* ldstab, const OutArgs a, const int wv) {
;     ...
;     for (int r = 0; r < 16; ++r) {
;         const int row = 32 * rb + crow(r, hi);
;         const float t1 = s1[r] + exch[((1 - dh) * 128 + row) * 2], t2 = s2[r] + exch[((1 - dh) * 128 + row) * 2 + 1];
;         float mean, inv;
;         if (MLSTM) { mean = 0.f; inv = rsqrtf(t2 * (1.f / DV) + EPS); }
;         else { mean = t1 * (1.f / DV); inv = rsqrtf(fmaxf(t2 * (1.f / DV) - mean * mean, 0.f) + EPS); }
; #pragma unroll
;         for (int nb = 0; nb < NB; ++nb) { const int col = dh * (DV / 2) + 32 * nb + r32;
;             *(LAS bf16_t*)(lds + row * TP + col * 2) = f2bf((o[nb][r] - mean) * inv); }
;     }
;     __syncthreads();
;     constexpr int CPR = DV / 8;
; #pragma unroll 1
;     for (int id = tid; id < 128 * CPR; id += 512) { const int row = id / CPR, ch = id % CPR;
;         const u32x4 y = *(const LAS u32x4*)(lds + row * TP + ch * 16);
;         const f32x4 g0 = *(const f32x4*)(a.gain + 8 * ch), g1 = *(const f32x4*)(a.gain + 8 * ch + 4);
	v_pk_add_f32 v[0:1], v[128:129], v[4:5]
	s_nop 0
	v_pk_mul_f32 v[0:1], v[0:1], s[36:37] op_sel_hi:[1,0]
	s_nop 0
	v_fma_f32 v1, -v0, v0, v1
	v_max_f32_e32 v1, 0, v1
	v_add_f32_e32 v1, 0x358637bd, v1
	v_mul_f32_e32 v4, 0x4b800000, v1
	v_cmp_gt_f32_e32 vcc, s89, v1
	s_nop 1
	v_cndmask_b32_e32 v1, v1, v4, vcc
	v_rsq_f32_e32 v1, v1
	v_bfe_u32 v4, v3, 16, 1
	v_add3_u32 v3, v3, v4, s90
	ds_write_b16_d16_hi v2, v3 offset:448
	v_mul_f32_e32 v2, 0x45800000, v1
	v_cndmask_b32_e32 v1, v1, v2, vcc
	v_sub_f32_e32 v3, v30, v0
	v_mul_f32_e32 v3, v3, v1
	v_lshlrev_b32_e32 v2, 10, v162
	v_bfe_u32 v4, v3, 16, 1
	v_add3_u32 v3, v3, v4, s90
	v_add3_u32 v2, 0, v2, v16
	ds_write_b16_d16_hi v2, v3
	v_sub_f32_e32 v3, v14, v0
	v_mul_f32_e32 v3, v3, v1
	v_bfe_u32 v4, v3, 16, 1
	v_add3_u32 v3, v3, v4, s90
	ds_write_b16_d16_hi v2, v3 offset:64
	v_sub_f32_e32 v3, v46, v0
	v_mul_f32_e32 v3, v3, v1
	v_bfe_u32 v4, v3, 16, 1
	v_add3_u32 v3, v3, v4, s90
	ds_write_b16_d16_hi v2, v3 offset:128
	v_sub_f32_e32 v3, v62, v0
	v_mul_f32_e32 v3, v3, v1
	v_bfe_u32 v4, v3, 16, 1
	v_add3_u32 v3, v3, v4, s90
	ds_write_b16_d16_hi v2, v3 offset:192
	v_sub_f32_e32 v3, v110, v0
	v_mul_f32_e32 v3, v3, v1
	v_bfe_u32 v4, v3, 16, 1
	v_add3_u32 v3, v3, v4, s90
	ds_write_b16_d16_hi v2, v3 offset:256
	v_sub_f32_e32 v3, v126, v0
	v_mul_f32_e32 v3, v3, v1
	v_bfe_u32 v4, v3, 16, 1
	v_add3_u32 v3, v3, v4, s90
	ds_write_b16_d16_hi v2, v3 offset:320
	v_sub_f32_e32 v3, v94, v0
	v_mul_f32_e32 v3, v3, v1
	v_bfe_u32 v4, v3, 16, 1
	v_add3_u32 v3, v3, v4, s90
	v_sub_f32_e32 v0, v78, v0
	ds_write_b16_d16_hi v2, v3 offset:384
	v_mul_f32_e32 v3, v0, v1
	v_pk_add_f32 v[0:1], v[130:131], v[6:7]
	s_nop 0
	v_pk_mul_f32 v[0:1], v[0:1], s[36:37] op_sel_hi:[1,0]
	s_nop 0
	v_fma_f32 v1, -v0, v0, v1
	v_max_f32_e32 v1, 0, v1
	v_add_f32_e32 v1, 0x358637bd, v1
	v_mul_f32_e32 v4, 0x4b800000, v1
	v_cmp_gt_f32_e32 vcc, s89, v1
	s_nop 1
	v_cndmask_b32_e32 v1, v1, v4, vcc
	v_rsq_f32_e32 v1, v1
	v_bfe_u32 v4, v3, 16, 1
	v_add3_u32 v3, v3, v4, s90
	ds_write_b16_d16_hi v2, v3 offset:448
	v_mul_f32_e32 v2, 0x45800000, v1
	v_cndmask_b32_e32 v1, v1, v2, vcc
	v_sub_f32_e32 v3, v31, v0
	v_mul_f32_e32 v3, v3, v1
	v_lshlrev_b32_e32 v2, 10, v160
	v_bfe_u32 v4, v3, 16, 1
	v_add3_u32 v3, v3, v4, s90
	v_add3_u32 v2, 0, v2, v16
	ds_write_b16_d16_hi v2, v3
	v_sub_f32_e32 v3, v15, v0
	v_mul_f32_e32 v3, v3, v1
	v_bfe_u32 v4, v3, 16, 1
	v_add3_u32 v3, v3, v4, s90
	ds_write_b16_d16_hi v2, v3 offset:64
	v_sub_f32_e32 v3, v47, v0
	v_mul_f32_e32 v3, v3, v1
	v_bfe_u32 v4, v3, 16, 1
	v_add3_u32 v3, v3, v4, s90
	ds_write_b16_d16_hi v2, v3 offset:128
	v_sub_f32_e32 v3, v63, v0
	v_mul_f32_e32 v3, v3, v1
	v_bfe_u32 v4, v3, 16, 1
	v_add3_u32 v3, v3, v4, s90
	ds_write_b16_d16_hi v2, v3 offset:192
	v_sub_f32_e32 v3, v111, v0
	v_mul_f32_e32 v3, v3, v1
	v_bfe_u32 v4, v3, 16, 1
	v_add3_u32 v3, v3, v4, s90
	ds_write_b16_d16_hi v2, v3 offset:256
	v_sub_f32_e32 v3, v127, v0
	v_mul_f32_e32 v3, v3, v1
	v_bfe_u32 v4, v3, 16, 1
	v_add3_u32 v3, v3, v4, s90
	ds_write_b16_d16_hi v2, v3 offset:320
	v_sub_f32_e32 v3, v95, v0
	v_sub_f32_e32 v0, v79, v0
	v_mul_f32_e32 v3, v3, v1
	v_mul_f32_e32 v0, v0, v1
	v_bfe_u32 v4, v3, 16, 1
	v_bfe_u32 v1, v0, 16, 1
	v_add3_u32 v3, v3, v4, s90
	v_add3_u32 v0, v0, v1, s90
	v_cmp_gt_i32_e32 vcc, s88, v232
	ds_write_b16_d16_hi v2, v3 offset:384
	ds_write_b16_d16_hi v2, v0 offset:448
	s_waitcnt lgkmcnt(0)
	s_barrier
	s_and_saveexec_b64 s[38:39], vcc
	s_cbranch_execz .LBB0_1826
	s_lshl_b32 s4, s8, 2
	s_add_u32 s40, s24, s4
	s_addc_u32 s41, s25, 0
	s_lshl_b64 s[2:3], s[2:3], 11
	s_add_u32 s4, s53, s2
	s_addc_u32 s5, s54, s3
	s_add_u32 s42, s4, s8
	s_addc_u32 s43, s5, 0
	s_add_u32 s2, s55, s2
	s_addc_u32 s3, s56, s3
	s_add_u32 s44, s2, s8
	s_addc_u32 s45, s3, 0
	v_lshl_add_u32 v4, v232, 4, 0
	v_lshlrev_b32_e32 v5, 3, v232
	s_mov_b64 s[46:47], 0
	v_and_b32_e32 v6, 63, v232
	v_lshrrev_b32_e32 v7, 6, v232
	v_lshlrev_b32_e32 v8, 5, v6
	v_lshlrev_b32_e32 v5, 3, v6
	v_lshl_add_u32 v5, v7, 11, v5
	global_load_dwordx4 v[40:43], v8, s[40:41]
	global_load_dwordx4 v[44:47], v8, s[40:41] offset:16
	v_mov_b32_e32 v162, v163
	s_movk_i32 s46, 16
; #define LAS __attribute__((address_space(3)))
; __device__ __forceinline__ float sigmoidf_(float x) { return 1.f / (1.f + __expf(-x)); }
; __device__ __forceinline__ float siluf_(float x) { return x / (1.f + __expf(-x)); }
; template <int DK, int DV, bool MLSTM>
; __device__ __forceinline__ void out_unit2(LAS unsigned char* lds, LAS unsigned char* ldstab, const OutArgs a, const int wv) {
;     ...
; #pragma unroll 1
;     for (int id = tid; id < 128 * CPR; id += 512) { const int row = id / CPR, ch = id % CPR;
;         const u32x4 y = *(const LAS u32x4*)(lds + row * TP + ch * 16);
;         const f32x4 g0 = *(const f32x4*)(a.gain + 8 * ch), g1 = *(const f32x4*)(a.gain + 8 * ch + 4);
;         float yv[8] = {bf_lo(y.x), bf_hi(y.x), bf_lo(y.y), bf_hi(y.y), bf_lo(y.z), bf_hi(y.z), bf_lo(y.w), bf_hi(y.w)};
;         float gv[8];
;         if (MLSTM) { const u32x4 g = *(const u32x4*)(a.G + (size_t)row * a.ldg + 8 * ch);
;             gv[0] = bf_lo(g.x); gv[1] = bf_hi(g.x); gv[2] = bf_lo(g.y); gv[3] = bf_hi(g.y); gv[4] = bf_lo(g.z); gv[5] = bf_hi(g.z); gv[6] = bf_lo(g.w); gv[7] = bf_hi(g.w); }
;         else { const u32x2 g = *(const u32x2*)(a.G8 + (size_t)row * a.ldg8 + 8 * ch);
;             const f32x2 e0 = __builtin_amdgcn_cvt_pk_f32_fp8((int)g.x, false), e1 = __builtin_amdgcn_cvt_pk_f32_fp8((int)g.x, true), e2 = __builtin_amdgcn_cvt_pk_f32_fp8((int)g.y, false), e3 = __builtin_amdgcn_cvt_pk_f32_fp8((int)g.y, true);
;             gv[0] = e0[0] * a.g8inv; gv[1] = e0[1] * a.g8inv; gv[2] = e1[0] * a.g8inv; gv[3] = e1[1] * a.g8inv; gv[4] = e2[0] * a.g8inv; gv[5] = e2[1] * a.g8inv; gv[6] = e3[0] * a.g8inv; gv[7] = e3[1] * a.g8inv; }
;         float gn[8] = {g0[0], g0[1], g0[2], g0[3], g1[0], g1[1], g1[2], g1[3]};
;         float ov[8];
; #pragma unroll
;         for (int i = 0; i < 8; ++i) ov[i] = yv[i] * gn[i] * (MLSTM ? sigmoidf_(gv[i]) : siluf_(gv[i]));
;         u32x2 w; w.x = pg8::pk4_fp8c(ov[0] * a.oscale, ov[1] * a.oscale, ov[2] * a.oscale, ov[3] * a.oscale); w.y = pg8::pk4_fp8c(ov[4] * a.oscale, ov[5] * a.oscale, ov[6] * a.oscale, ov[7] * a.oscale);
;         *(u32x2*)(a.Out + (size_t)row * a.ldo + 8 * ch) = w; }
.Ldloop0:
	ds_read_b128 v[0:3], v4
	global_load_dwordx2 v[30:31], v5, s[42:43]
	v_add_u32_e32 v4, 0x2000, v4
	s_waitcnt lgkmcnt(0)
	v_lshlrev_b32_e32 v10, 16, v0
	v_and_b32_e32 v11, 0xffff0000, v0
	v_lshlrev_b32_e32 v12, 16, v1
	v_and_b32_e32 v13, 0xffff0000, v1
	v_lshlrev_b32_e32 v14, 16, v2
	v_and_b32_e32 v15, 0xffff0000, v2
	v_lshlrev_b32_e32 v16, 16, v3
	v_and_b32_e32 v17, 0xffff0000, v3
	s_waitcnt vmcnt(0)
	v_cvt_pk_f32_fp8_e32 v[32:33], v30
	v_cvt_pk_f32_fp8_sdwa v[34:35], v30 src0_sel:WORD_1
	v_cvt_pk_f32_fp8_e32 v[36:37], v31
	v_cvt_pk_f32_fp8_sdwa v[38:39], v31 src0_sel:WORD_1
	v_pk_mul_f32 v[10:11], v[40:41], v[10:11]
	v_pk_mul_f32 v[12:13], v[42:43], v[12:13]
	v_pk_mul_f32 v[14:15], v[44:45], v[14:15]
	v_pk_mul_f32 v[16:17], v[46:47], v[16:17]
	v_pk_mul_f32 v[32:33], v[32:33], v[162:163]
	v_pk_mul_f32 v[34:35], v[34:35], v[162:163]
	v_pk_mul_f32 v[36:37], v[36:37], v[162:163]
	v_pk_mul_f32 v[38:39], v[38:39], v[162:163]
	v_mul_f32_e32 v48, 0xbfb8aa3b, v32
	v_mul_f32_e32 v49, 0xbfb8aa3b, v33
	v_mul_f32_e32 v50, 0xbfb8aa3b, v34
	v_mul_f32_e32 v51, 0xbfb8aa3b, v35
	v_mul_f32_e32 v52, 0xbfb8aa3b, v36
	v_mul_f32_e32 v53, 0xbfb8aa3b, v37
	v_mul_f32_e32 v54, 0xbfb8aa3b, v38
	v_mul_f32_e32 v55, 0xbfb8aa3b, v39
	v_exp_f32_e32 v48, v48
	v_exp_f32_e32 v49, v49
	v_exp_f32_e32 v50, v50
	v_exp_f32_e32 v51, v51
	v_exp_f32_e32 v52, v52
	v_exp_f32_e32 v53, v53
	v_exp_f32_e32 v54, v54
	v_exp_f32_e32 v55, v55
	v_add_f32_e32 v48, 1.0, v48
	v_add_f32_e32 v49, 1.0, v49
	v_add_f32_e32 v50, 1.0, v50
	v_add_f32_e32 v51, 1.0, v51
	v_add_f32_e32 v52, 1.0, v52
	v_add_f32_e32 v53, 1.0, v53
	v_add_f32_e32 v54, 1.0, v54
	v_add_f32_e32 v55, 1.0, v55
	v_rcp_f32_e32 v56, v48
	v_rcp_f32_e32 v57, v49
	v_rcp_f32_e32 v58, v50
	v_rcp_f32_e32 v59, v51
	v_rcp_f32_e32 v60, v52
	v_rcp_f32_e32 v61, v53
	v_rcp_f32_e32 v62, v54
	v_rcp_f32_e32 v63, v55
	v_fma_f32 v0, -v48, v56, 1.0
	v_fma_f32 v1, -v49, v57, 1.0
	v_fma_f32 v2, -v50, v58, 1.0
	v_fma_f32 v3, -v51, v59, 1.0
	v_fma_f32 v6, -v52, v60, 1.0
	v_fma_f32 v7, -v53, v61, 1.0
	v_fma_f32 v8, -v54, v62, 1.0
	v_fma_f32 v9, -v55, v63, 1.0
	v_fmac_f32_e32 v56, v0, v56
	v_fmac_f32_e32 v57, v1, v57
	v_fmac_f32_e32 v58, v2, v58
	v_fmac_f32_e32 v59, v3, v59
	v_fmac_f32_e32 v60, v6, v60
	v_fmac_f32_e32 v61, v7, v61
	v_fmac_f32_e32 v62, v8, v62
	v_fmac_f32_e32 v63, v9, v63
	v_mul_f32_e32 v64, v32, v56
	v_mul_f32_e32 v65, v33, v57
	v_mul_f32_e32 v66, v34, v58
	v_mul_f32_e32 v67, v35, v59
	v_mul_f32_e32 v68, v36, v60
	v_mul_f32_e32 v69, v37, v61
	v_mul_f32_e32 v70, v38, v62
	v_mul_f32_e32 v71, v39, v63
	v_fma_f32 v0, -v48, v64, v32
	v_fma_f32 v1, -v49, v65, v33
	v_fma_f32 v2, -v50, v66, v34
	v_fma_f32 v3, -v51, v67, v35
	v_fma_f32 v6, -v52, v68, v36
	v_fma_f32 v7, -v53, v69, v37
	v_fma_f32 v8, -v54, v70, v38
	v_fma_f32 v9, -v55, v71, v39
	v_fmac_f32_e32 v64, v0, v56
	v_fmac_f32_e32 v65, v1, v57
	v_fmac_f32_e32 v66, v2, v58
	v_fmac_f32_e32 v67, v3, v59
	v_fmac_f32_e32 v68, v6, v60
	v_fmac_f32_e32 v69, v7, v61
	v_fmac_f32_e32 v70, v8, v62
	v_fmac_f32_e32 v71, v9, v63
	v_fma_f32 v0, -v48, v64, v32
	v_fma_f32 v1, -v49, v65, v33
	v_fma_f32 v2, -v50, v66, v34
	v_fma_f32 v3, -v51, v67, v35
	v_fma_f32 v6, -v52, v68, v36
	v_fma_f32 v7, -v53, v69, v37
	v_fma_f32 v8, -v54, v70, v38
	v_fma_f32 v9, -v55, v71, v39
	v_fma_f32 v0, v0, v56, v64
	v_fma_f32 v1, v1, v57, v65
	v_fma_f32 v2, v2, v58, v66
	v_fma_f32 v3, v3, v59, v67
	v_fma_f32 v6, v6, v60, v68
	v_fma_f32 v7, v7, v61, v69
	v_fma_f32 v8, v8, v62, v70
	v_fma_f32 v9, v9, v63, v71
	v_div_fixup_f32 v0, v0, v48, v32
	v_div_fixup_f32 v1, v1, v49, v33
	v_div_fixup_f32 v2, v2, v50, v34
	v_div_fixup_f32 v3, v3, v51, v35
	v_div_fixup_f32 v6, v6, v52, v36
	v_div_fixup_f32 v7, v7, v53, v37
	v_div_fixup_f32 v8, v8, v54, v38
	v_div_fixup_f32 v9, v9, v55, v39
	v_mul_f32_e32 v10, v10, v0
	v_mul_f32_e32 v11, v11, v1
	v_mul_f32_e32 v12, v12, v2
	v_mul_f32_e32 v13, v13, v3
	v_mul_f32_e32 v14, v14, v6
	v_mul_f32_e32 v15, v15, v7
	v_mul_f32_e32 v16, v16, v8
	v_mul_f32_e32 v17, v17, v9
	v_mul_f32_e32 v10, 0x41800000, v10
	v_mul_f32_e32 v11, 0x41800000, v11
	v_mul_f32_e32 v12, 0x41800000, v12
	v_mul_f32_e32 v13, 0x41800000, v13
	v_mul_f32_e32 v14, 0x41800000, v14
	v_mul_f32_e32 v15, 0x41800000, v15
	v_mul_f32_e32 v16, 0x41800000, v16
	v_mul_f32_e32 v17, 0x41800000, v17
	v_med3_f32 v10, v10, s91, v231
	v_med3_f32 v11, v11, s91, v231
	v_med3_f32 v12, v12, s91, v231
	v_med3_f32 v13, v13, s91, v231
	v_med3_f32 v14, v14, s91, v231
	v_med3_f32 v15, v15, s91, v231
	v_med3_f32 v16, v16, s91, v231
	v_med3_f32 v17, v17, s91, v231
	v_cvt_pk_fp8_f32 v24, v10, v11
	v_cvt_pk_fp8_f32 v25, v14, v15
	s_nop 0
	v_cvt_pk_fp8_f32 v24, v12, v13 op_sel:[0,0,1]
	v_cvt_pk_fp8_f32 v25, v16, v17 op_sel:[0,0,1]
	s_add_i32 s46, s46, -1
	s_cmp_lg_u32 s46, 0
	s_nop 0
	global_store_dwordx2 v5, v[24:25], s[44:45]
	v_add_u32_e32 v5, 0x4000, v5
	s_cbranch_scc1 .Ldloop0
	s_branch .LBB0_1826

; #define LAS __attribute__((address_space(3)))
; __device__ __forceinline__ bf16_t f2bf(float f) { unsigned u = __builtin_bit_cast(unsigned, f); return (bf16_t)((u + 0x7fffu + ((u >> 16) & 1u)) >> 16); }
; __device__ __forceinline__ int crow(int r, int hi) { return (r & 3) + 8 * (r >> 2) + 4 * hi; }
; __device__ __forceinline__ int crow(int r, int hi) { return (r & 3) + 8 * (r >> 2) + 4 * hi; }
; template <int DK, int DV, bool MLSTM>
; __device__ __forceinline__ void out_unit2(LAS unsigned char* lds, LAS unsigned char* ldstab, const OutArgs a, const int wv) {
;     ...
;     __syncthreads();
;     constexpr int TP = DV * 2;
;     static_assert(128 * TP <= 2 * NPK * 32768, "output tile fits the Q + K regions");
; #pragma unroll
;     for (int r = 0; r < 16; ++r) {
;         const int row = 32 * rb + crow(r, hi);
;         const float t1 = s1[r] + exch[((1 - dh) * 128 + row) * 2], t2 = s2[r] + exch[((1 - dh) * 128 + row) * 2 + 1];
;         float mean, inv;
;         if (MLSTM) { mean = 0.f; inv = rsqrtf(t2 * (1.f / DV) + EPS); }
;         else { mean = t1 * (1.f / DV); inv = rsqrtf(fmaxf(t2 * (1.f / DV) - mean * mean, 0.f) + EPS); }
; #pragma unroll
;         for (int nb = 0; nb < NB; ++nb) { const int col = dh * (DV / 2) + 32 * nb + r32;
;             *(LAS bf16_t*)(lds + row * TP + col * 2) = f2bf((o[nb][r] - mean) * inv); }
.LBB0_4313:
	s_or_b64 exec, exec, s[4:5]
	v_lshlrev_b32_e32 v164, 1, v219
	v_subrev_u32_e32 v164, s6, v164
	s_add_i32 s4, 0, 0x22100
	v_lshl_add_u32 v164, v164, 2, s4
	s_waitcnt vmcnt(0) lgkmcnt(0)
	s_barrier
	ds_read_b128 v[164:167], v164 offset:1024
	v_lshlrev_b32_e32 v168, 1, v217
	v_subrev_u32_e32 v168, s6, v168
	v_lshl_add_u32 v168, v168, 2, s4
	ds_read2_b64 v[168:171], v168 offset0:128 offset1:129
	s_waitcnt lgkmcnt(1)
	v_pk_add_f32 v[156:157], v[156:157], v[164:165]
	s_nop 0
	v_pk_mul_f32 v[156:157], v[156:157], s[26:27] op_sel_hi:[1,0]
	s_nop 0
	v_fma_f32 v157, -v156, v156, v157
	v_max_f32_e32 v157, 0, v157
	v_add_f32_e32 v157, 0x358637bd, v157
	v_mul_f32_e32 v164, 0x4b800000, v157
	v_cmp_gt_f32_e32 vcc, s89, v157
	v_sub_f32_e32 v16, v16, v156
	v_sub_f32_e32 v0, v0, v156
	v_cndmask_b32_e32 v157, v157, v164, vcc
	v_rsq_f32_e32 v157, v157
	v_or_b32_e32 v164, s6, v233
	v_mul_f32_e32 v165, 0x45800000, v157
	v_cndmask_b32_e32 v157, v157, v165, vcc
	v_mul_f32_e32 v16, v16, v157
	v_bfe_u32 v172, v16, 16, 1
	v_lshlrev_b32_e32 v165, 10, v219
	v_add3_u32 v172, v16, v172, s90
	v_lshlrev_b32_e32 v16, 1, v164
	v_mul_f32_e32 v0, v0, v157
	v_add3_u32 v164, 0, v165, v16
	v_bfe_u32 v165, v0, 16, 1
	v_add3_u32 v0, v0, v165, s90
	ds_write_b16_d16_hi v164, v0 offset:64
	v_sub_f32_e32 v0, v32, v156
	v_mul_f32_e32 v0, v0, v157
	v_bfe_u32 v32, v0, 16, 1
	v_add3_u32 v0, v0, v32, s90
	ds_write_b16_d16_hi v164, v0 offset:128
	v_sub_f32_e32 v0, v48, v156
	v_mul_f32_e32 v0, v0, v157
	v_bfe_u32 v32, v0, 16, 1
	v_add3_u32 v0, v0, v32, s90
	ds_write_b16_d16_hi v164, v0 offset:192
	v_sub_f32_e32 v0, v96, v156
	v_mul_f32_e32 v0, v0, v157
	v_bfe_u32 v32, v0, 16, 1
	v_add3_u32 v0, v0, v32, s90
	ds_write_b16_d16_hi v164, v0 offset:256
	v_sub_f32_e32 v0, v112, v156
	v_mul_f32_e32 v0, v0, v157
	v_bfe_u32 v32, v0, 16, 1
	v_add3_u32 v0, v0, v32, s90
	ds_write_b16_d16_hi v164, v0 offset:320
	v_sub_f32_e32 v0, v80, v156
	v_mul_f32_e32 v0, v0, v157
	v_bfe_u32 v32, v0, 16, 1
	v_add3_u32 v0, v0, v32, s90
	ds_write_b16_d16_hi v164, v0 offset:384
	v_sub_f32_e32 v0, v64, v156
	v_mul_f32_e32 v0, v0, v157
	v_pk_add_f32 v[156:157], v[158:159], v[166:167]
	ds_write_b16_d16_hi v164, v172
	v_pk_mul_f32 v[156:157], v[156:157], s[26:27] op_sel_hi:[1,0]
	s_nop 0
	v_fma_f32 v32, -v156, v156, v157
	v_max_f32_e32 v32, 0, v32
	v_add_f32_e32 v32, 0x358637bd, v32
	v_mul_f32_e32 v48, 0x4b800000, v32
	v_cmp_gt_f32_e32 vcc, s89, v32
	v_sub_f32_e32 v17, v17, v156
	v_sub_f32_e32 v1, v1, v156
	v_cndmask_b32_e32 v32, v32, v48, vcc
	v_rsq_f32_e32 v32, v32
	v_bfe_u32 v48, v0, 16, 1
	v_add3_u32 v0, v0, v48, s90
	ds_write_b16_d16_hi v164, v0 offset:448
	v_mul_f32_e32 v0, 0x45800000, v32
	v_cndmask_b32_e32 v0, v32, v0, vcc
	v_mul_f32_e32 v17, v17, v0
	v_lshlrev_b32_e32 v32, 10, v218
	v_bfe_u32 v48, v17, 16, 1
	v_add3_u32 v17, v17, v48, s90
	v_add3_u32 v32, 0, v32, v16
	v_mul_f32_e32 v1, v1, v0
	ds_write_b16_d16_hi v32, v17
	v_bfe_u32 v17, v1, 16, 1
	v_add3_u32 v1, v1, v17, s90
	ds_write_b16_d16_hi v32, v1 offset:64
	v_sub_f32_e32 v1, v33, v156
	v_mul_f32_e32 v1, v1, v0
	v_bfe_u32 v17, v1, 16, 1
	v_add3_u32 v1, v1, v17, s90
	ds_write_b16_d16_hi v32, v1 offset:128
	v_sub_f32_e32 v1, v49, v156
	v_mul_f32_e32 v1, v1, v0
	v_bfe_u32 v17, v1, 16, 1
	v_add3_u32 v1, v1, v17, s90
	ds_write_b16_d16_hi v32, v1 offset:192
	v_sub_f32_e32 v1, v97, v156
	v_mul_f32_e32 v1, v1, v0
	v_bfe_u32 v17, v1, 16, 1
	v_add3_u32 v1, v1, v17, s90
	ds_write_b16_d16_hi v32, v1 offset:256
	v_sub_f32_e32 v1, v113, v156
	v_mul_f32_e32 v1, v1, v0
	v_bfe_u32 v17, v1, 16, 1
	v_add3_u32 v1, v1, v17, s90
	ds_write_b16_d16_hi v32, v1 offset:320
	v_sub_f32_e32 v1, v81, v156
	v_mul_f32_e32 v1, v1, v0
	v_bfe_u32 v17, v1, 16, 1
	v_add3_u32 v1, v1, v17, s90
	ds_write_b16_d16_hi v32, v1 offset:384
	v_sub_f32_e32 v1, v65, v156
	v_mul_f32_e32 v17, v1, v0
	s_waitcnt lgkmcnt(14)
	v_pk_add_f32 v[0:1], v[152:153], v[168:169]
	s_nop 0
	v_pk_mul_f32 v[0:1], v[0:1], s[26:27] op_sel_hi:[1,0]
	s_nop 0
	v_fma_f32 v1, -v0, v0, v1
	v_max_f32_e32 v1, 0, v1
	v_add_f32_e32 v1, 0x358637bd, v1
	v_mul_f32_e32 v33, 0x4b800000, v1
	v_cmp_gt_f32_e32 vcc, s89, v1
	v_sub_f32_e32 v18, v18, v0
	v_sub_f32_e32 v2, v2, v0
	v_cndmask_b32_e32 v1, v1, v33, vcc
	v_rsq_f32_e32 v1, v1
	v_bfe_u32 v33, v17, 16, 1
	v_add3_u32 v17, v17, v33, s90
	ds_write_b16_d16_hi v32, v17 offset:448
	v_mul_f32_e32 v17, 0x45800000, v1
	v_cndmask_b32_e32 v1, v1, v17, vcc
	v_mul_f32_e32 v18, v18, v1
	v_lshlrev_b32_e32 v17, 10, v217
	v_bfe_u32 v32, v18, 16, 1
	v_add3_u32 v18, v18, v32, s90
	v_add3_u32 v17, 0, v17, v16
	v_mul_f32_e32 v2, v2, v1
	ds_write_b16_d16_hi v17, v18
	v_bfe_u32 v18, v2, 16, 1
	v_add3_u32 v2, v2, v18, s90
	ds_write_b16_d16_hi v17, v2 offset:64
	v_sub_f32_e32 v2, v34, v0
	v_mul_f32_e32 v2, v2, v1
	v_bfe_u32 v18, v2, 16, 1
	v_add3_u32 v2, v2, v18, s90
	ds_write_b16_d16_hi v17, v2 offset:128
	v_sub_f32_e32 v2, v50, v0
	v_mul_f32_e32 v2, v2, v1
	v_bfe_u32 v18, v2, 16, 1
	v_add3_u32 v2, v2, v18, s90
	ds_write_b16_d16_hi v17, v2 offset:192
	v_sub_f32_e32 v2, v98, v0
	v_mul_f32_e32 v2, v2, v1
	v_bfe_u32 v18, v2, 16, 1
	v_add3_u32 v2, v2, v18, s90
	ds_write_b16_d16_hi v17, v2 offset:256
	v_sub_f32_e32 v2, v114, v0
	v_mul_f32_e32 v2, v2, v1
	v_bfe_u32 v18, v2, 16, 1
	v_add3_u32 v2, v2, v18, s90
	ds_write_b16_d16_hi v17, v2 offset:320
	v_sub_f32_e32 v2, v82, v0
	v_mul_f32_e32 v2, v2, v1
	v_bfe_u32 v18, v2, 16, 1
	v_add3_u32 v2, v2, v18, s90
	v_sub_f32_e32 v0, v66, v0
	ds_write_b16_d16_hi v17, v2 offset:384
	v_mul_f32_e32 v2, v0, v1
	v_pk_add_f32 v[0:1], v[154:155], v[170:171]
	s_nop 0
	v_pk_mul_f32 v[0:1], v[0:1], s[26:27] op_sel_hi:[1,0]
	s_nop 0
	v_fma_f32 v1, -v0, v0, v1
	v_max_f32_e32 v1, 0, v1
; #define LAS __attribute__((address_space(3)))
; __device__ __forceinline__ bf16_t f2bf(float f) { unsigned u = __builtin_bit_cast(unsigned, f); return (bf16_t)((u + 0x7fffu + ((u >> 16) & 1u)) >> 16); }
; __device__ __forceinline__ int crow(int r, int hi) { return (r & 3) + 8 * (r >> 2) + 4 * hi; }
; __device__ __forceinline__ int crow(int r, int hi) { return (r & 3) + 8 * (r >> 2) + 4 * hi; }
; template <int DK, int DV, bool MLSTM>
; __device__ __forceinline__ void out_unit2(LAS unsigned char* lds, LAS unsigned char* ldstab, const OutArgs a, const int wv) {
;     ...
;     for (int r = 0; r < 16; ++r) {
;         const int row = 32 * rb + crow(r, hi);
;         const float t1 = s1[r] + exch[((1 - dh) * 128 + row) * 2], t2 = s2[r] + exch[((1 - dh) * 128 + row) * 2 + 1];
;         float mean, inv;
;         if (MLSTM) { mean = 0.f; inv = rsqrtf(t2 * (1.f / DV) + EPS); }
;         else { mean = t1 * (1.f / DV); inv = rsqrtf(fmaxf(t2 * (1.f / DV) - mean * mean, 0.f) + EPS); }
; #pragma unroll
;         for (int nb = 0; nb < NB; ++nb) { const int col = dh * (DV / 2) + 32 * nb + r32;
;             *(LAS bf16_t*)(lds + row * TP + col * 2) = f2bf((o[nb][r] - mean) * inv); }
	v_add_f32_e32 v1, 0x358637bd, v1
	v_mul_f32_e32 v18, 0x4b800000, v1
	v_cmp_gt_f32_e32 vcc, s89, v1
	s_nop 1
	v_cndmask_b32_e32 v1, v1, v18, vcc
	v_rsq_f32_e32 v1, v1
	v_bfe_u32 v18, v2, 16, 1
	v_add3_u32 v2, v2, v18, s90
	ds_write_b16_d16_hi v17, v2 offset:448
	v_mul_f32_e32 v2, 0x45800000, v1
	v_cndmask_b32_e32 v1, v1, v2, vcc
	v_sub_f32_e32 v17, v19, v0
	v_mul_f32_e32 v17, v17, v1
	v_lshlrev_b32_e32 v2, 10, v216
	v_bfe_u32 v18, v17, 16, 1
	v_add3_u32 v17, v17, v18, s90
	v_add3_u32 v18, 0, v2, v16
	v_sub_f32_e32 v2, v3, v0
	v_mul_f32_e32 v2, v2, v1
	v_bfe_u32 v3, v2, 16, 1
	v_add3_u32 v2, v2, v3, s90
	ds_write_b16_d16_hi v18, v2 offset:64
	v_sub_f32_e32 v2, v35, v0
	v_mul_f32_e32 v2, v2, v1
	v_bfe_u32 v3, v2, 16, 1
	v_add3_u32 v2, v2, v3, s90
	ds_write_b16_d16_hi v18, v2 offset:128
	v_sub_f32_e32 v2, v51, v0
	v_mul_f32_e32 v2, v2, v1
	v_bfe_u32 v3, v2, 16, 1
	v_add3_u32 v2, v2, v3, s90
	ds_write_b16_d16_hi v18, v2 offset:192
	v_sub_f32_e32 v2, v99, v0
	v_mul_f32_e32 v2, v2, v1
	v_bfe_u32 v3, v2, 16, 1
	v_add3_u32 v2, v2, v3, s90
	ds_write_b16_d16_hi v18, v2 offset:256
	v_sub_f32_e32 v2, v115, v0
	v_mul_f32_e32 v2, v2, v1
	v_bfe_u32 v3, v2, 16, 1
	v_add3_u32 v2, v2, v3, s90
	ds_write_b16_d16_hi v18, v2 offset:320
	v_sub_f32_e32 v2, v83, v0
	v_sub_f32_e32 v0, v67, v0
	ds_write_b16_d16_hi v18, v17
	v_mul_f32_e32 v2, v2, v1
	v_mul_f32_e32 v17, v0, v1
	v_lshlrev_b32_e32 v0, 1, v215
	v_bfe_u32 v3, v2, 16, 1
	v_subrev_u32_e32 v0, s6, v0
	v_add3_u32 v2, v2, v3, s90
	v_lshl_add_u32 v0, v0, 2, s4
	ds_write_b16_d16_hi v18, v2 offset:384
	ds_read2_b64 v[0:3], v0 offset0:128 offset1:129
	v_lshlrev_b32_e32 v19, 1, v213
	v_subrev_u32_e32 v19, s6, v19
	v_lshl_add_u32 v19, v19, 2, s4
	ds_read2_b64 v[32:35], v19 offset0:128 offset1:129
	s_waitcnt lgkmcnt(1)
	v_pk_add_f32 v[0:1], v[148:149], v[0:1]
	s_nop 0
	v_pk_mul_f32 v[0:1], v[0:1], s[26:27] op_sel_hi:[1,0]
	s_nop 0
	v_fma_f32 v1, -v0, v0, v1
	v_max_f32_e32 v1, 0, v1
	v_add_f32_e32 v1, 0x358637bd, v1
	v_mul_f32_e32 v19, 0x4b800000, v1
	v_cmp_gt_f32_e32 vcc, s89, v1
	v_sub_f32_e32 v4, v4, v0
	s_nop 0
	v_cndmask_b32_e32 v1, v1, v19, vcc
	v_rsq_f32_e32 v1, v1
	v_bfe_u32 v19, v17, 16, 1
	v_add3_u32 v17, v17, v19, s90
	ds_write_b16_d16_hi v18, v17 offset:448
	v_mul_f32_e32 v17, 0x45800000, v1
	v_cndmask_b32_e32 v1, v1, v17, vcc
	v_sub_f32_e32 v18, v20, v0
	v_mul_f32_e32 v18, v18, v1
	v_lshlrev_b32_e32 v17, 10, v215
	v_bfe_u32 v19, v18, 16, 1
	v_add3_u32 v18, v18, v19, s90
	v_add3_u32 v17, 0, v17, v16
	v_mul_f32_e32 v4, v4, v1
	ds_write_b16_d16_hi v17, v18
	v_bfe_u32 v18, v4, 16, 1
	v_add3_u32 v4, v4, v18, s90
	ds_write_b16_d16_hi v17, v4 offset:64
	v_sub_f32_e32 v4, v36, v0
	v_mul_f32_e32 v4, v4, v1
	v_bfe_u32 v18, v4, 16, 1
	v_add3_u32 v4, v4, v18, s90
	ds_write_b16_d16_hi v17, v4 offset:128
	v_sub_f32_e32 v4, v52, v0
	v_mul_f32_e32 v4, v4, v1
	v_bfe_u32 v18, v4, 16, 1
	v_add3_u32 v4, v4, v18, s90
	ds_write_b16_d16_hi v17, v4 offset:192
	v_sub_f32_e32 v4, v100, v0
	v_mul_f32_e32 v4, v4, v1
	v_bfe_u32 v18, v4, 16, 1
	v_add3_u32 v4, v4, v18, s90
	ds_write_b16_d16_hi v17, v4 offset:256
	v_sub_f32_e32 v4, v116, v0
	v_mul_f32_e32 v4, v4, v1
	v_bfe_u32 v18, v4, 16, 1
	v_add3_u32 v4, v4, v18, s90
	ds_write_b16_d16_hi v17, v4 offset:320
	v_sub_f32_e32 v4, v84, v0
	v_mul_f32_e32 v4, v4, v1
	v_bfe_u32 v18, v4, 16, 1
	v_add3_u32 v4, v4, v18, s90
	v_sub_f32_e32 v0, v68, v0
	ds_write_b16_d16_hi v17, v4 offset:384
	v_mul_f32_e32 v4, v0, v1
	v_pk_add_f32 v[0:1], v[150:151], v[2:3]
	s_nop 0
	v_pk_mul_f32 v[0:1], v[0:1], s[26:27] op_sel_hi:[1,0]
	s_nop 0
	v_fma_f32 v1, -v0, v0, v1
	v_max_f32_e32 v1, 0, v1
	v_add_f32_e32 v1, 0x358637bd, v1
	v_mul_f32_e32 v2, 0x4b800000, v1
	v_cmp_gt_f32_e32 vcc, s89, v1
	v_sub_f32_e32 v3, v21, v0
	s_nop 0
	v_cndmask_b32_e32 v1, v1, v2, vcc
	v_rsq_f32_e32 v1, v1
	v_bfe_u32 v2, v4, 16, 1
	v_add3_u32 v2, v4, v2, s90
	ds_write_b16_d16_hi v17, v2 offset:448
	v_mul_f32_e32 v2, 0x45800000, v1
	v_cndmask_b32_e32 v1, v1, v2, vcc
	v_mul_f32_e32 v3, v3, v1
	v_lshlrev_b32_e32 v2, 10, v214
	v_bfe_u32 v4, v3, 16, 1
	v_add3_u32 v3, v3, v4, s90
	v_add3_u32 v2, 0, v2, v16
	ds_write_b16_d16_hi v2, v3
	v_sub_f32_e32 v3, v5, v0
	v_mul_f32_e32 v3, v3, v1
	v_bfe_u32 v4, v3, 16, 1
	v_add3_u32 v3, v3, v4, s90
	ds_write_b16_d16_hi v2, v3 offset:64
	v_sub_f32_e32 v3, v37, v0
	v_mul_f32_e32 v3, v3, v1
	v_bfe_u32 v4, v3, 16, 1
	v_add3_u32 v3, v3, v4, s90
	ds_write_b16_d16_hi v2, v3 offset:128
	v_sub_f32_e32 v3, v53, v0
	v_mul_f32_e32 v3, v3, v1
	v_bfe_u32 v4, v3, 16, 1
	v_add3_u32 v3, v3, v4, s90
	ds_write_b16_d16_hi v2, v3 offset:192
	v_sub_f32_e32 v3, v101, v0
	v_mul_f32_e32 v3, v3, v1
	v_bfe_u32 v4, v3, 16, 1
	v_add3_u32 v3, v3, v4, s90
	ds_write_b16_d16_hi v2, v3 offset:256
	v_sub_f32_e32 v3, v117, v0
	v_mul_f32_e32 v3, v3, v1
	v_bfe_u32 v4, v3, 16, 1
	v_add3_u32 v3, v3, v4, s90
	ds_write_b16_d16_hi v2, v3 offset:320
	v_sub_f32_e32 v3, v85, v0
	v_mul_f32_e32 v3, v3, v1
	v_bfe_u32 v4, v3, 16, 1
	v_add3_u32 v3, v3, v4, s90
	v_sub_f32_e32 v0, v69, v0
	ds_write_b16_d16_hi v2, v3 offset:384
	v_mul_f32_e32 v3, v0, v1
	s_waitcnt lgkmcnt(14)
; #define LAS __attribute__((address_space(3)))
; __device__ __forceinline__ bf16_t f2bf(float f) { unsigned u = __builtin_bit_cast(unsigned, f); return (bf16_t)((u + 0x7fffu + ((u >> 16) & 1u)) >> 16); }
; __device__ __forceinline__ int crow(int r, int hi) { return (r & 3) + 8 * (r >> 2) + 4 * hi; }
; __device__ __forceinline__ int crow(int r, int hi) { return (r & 3) + 8 * (r >> 2) + 4 * hi; }
; template <int DK, int DV, bool MLSTM>
; __device__ __forceinline__ void out_unit2(LAS unsigned char* lds, LAS unsigned char* ldstab, const OutArgs a, const int wv) {
;     ...
;     for (int r = 0; r < 16; ++r) {
;         const int row = 32 * rb + crow(r, hi);
;         const float t1 = s1[r] + exch[((1 - dh) * 128 + row) * 2], t2 = s2[r] + exch[((1 - dh) * 128 + row) * 2 + 1];
;         float mean, inv;
;         if (MLSTM) { mean = 0.f; inv = rsqrtf(t2 * (1.f / DV) + EPS); }
;         else { mean = t1 * (1.f / DV); inv = rsqrtf(fmaxf(t2 * (1.f / DV) - mean * mean, 0.f) + EPS); }
; #pragma unroll
;         for (int nb = 0; nb < NB; ++nb) { const int col = dh * (DV / 2) + 32 * nb + r32;
;             *(LAS bf16_t*)(lds + row * TP + col * 2) = f2bf((o[nb][r] - mean) * inv); }
	v_pk_add_f32 v[0:1], v[144:145], v[32:33]
	s_nop 0
	v_pk_mul_f32 v[0:1], v[0:1], s[26:27] op_sel_hi:[1,0]
	s_nop 0
	v_fma_f32 v1, -v0, v0, v1
	v_max_f32_e32 v1, 0, v1
	v_add_f32_e32 v1, 0x358637bd, v1
	v_mul_f32_e32 v4, 0x4b800000, v1
	v_cmp_gt_f32_e32 vcc, s89, v1
	s_nop 1
	v_cndmask_b32_e32 v1, v1, v4, vcc
	v_rsq_f32_e32 v1, v1
	v_bfe_u32 v4, v3, 16, 1
	v_add3_u32 v3, v3, v4, s90
	ds_write_b16_d16_hi v2, v3 offset:448
	v_mul_f32_e32 v2, 0x45800000, v1
	v_cndmask_b32_e32 v1, v1, v2, vcc
	v_sub_f32_e32 v3, v22, v0
	v_mul_f32_e32 v3, v3, v1
	v_lshlrev_b32_e32 v2, 10, v213
	v_bfe_u32 v4, v3, 16, 1
	v_add3_u32 v3, v3, v4, s90
	v_add3_u32 v2, 0, v2, v16
	ds_write_b16_d16_hi v2, v3
	v_sub_f32_e32 v3, v6, v0
	v_mul_f32_e32 v3, v3, v1
	v_bfe_u32 v4, v3, 16, 1
	v_add3_u32 v3, v3, v4, s90
	ds_write_b16_d16_hi v2, v3 offset:64
	v_sub_f32_e32 v3, v38, v0
	v_mul_f32_e32 v3, v3, v1
	v_bfe_u32 v4, v3, 16, 1
	v_add3_u32 v3, v3, v4, s90
	ds_write_b16_d16_hi v2, v3 offset:128
	v_sub_f32_e32 v3, v54, v0
	v_mul_f32_e32 v3, v3, v1
	v_bfe_u32 v4, v3, 16, 1
	v_add3_u32 v3, v3, v4, s90
	ds_write_b16_d16_hi v2, v3 offset:192
	v_sub_f32_e32 v3, v102, v0
	v_mul_f32_e32 v3, v3, v1
	v_bfe_u32 v4, v3, 16, 1
	v_add3_u32 v3, v3, v4, s90
	ds_write_b16_d16_hi v2, v3 offset:256
	v_sub_f32_e32 v3, v118, v0
	v_mul_f32_e32 v3, v3, v1
	v_bfe_u32 v4, v3, 16, 1
	v_add3_u32 v3, v3, v4, s90
	ds_write_b16_d16_hi v2, v3 offset:320
	v_sub_f32_e32 v3, v86, v0
	v_mul_f32_e32 v3, v3, v1
	v_bfe_u32 v4, v3, 16, 1
	v_add3_u32 v3, v3, v4, s90
	v_sub_f32_e32 v0, v70, v0
	ds_write_b16_d16_hi v2, v3 offset:384
	v_mul_f32_e32 v3, v0, v1
	v_pk_add_f32 v[0:1], v[146:147], v[34:35]
	s_nop 0
	v_pk_mul_f32 v[0:1], v[0:1], s[26:27] op_sel_hi:[1,0]
	s_nop 0
	v_fma_f32 v1, -v0, v0, v1
	v_max_f32_e32 v1, 0, v1
	v_add_f32_e32 v1, 0x358637bd, v1
	v_mul_f32_e32 v4, 0x4b800000, v1
	v_cmp_gt_f32_e32 vcc, s89, v1
	s_nop 1
	v_cndmask_b32_e32 v1, v1, v4, vcc
	v_rsq_f32_e32 v1, v1
	v_bfe_u32 v4, v3, 16, 1
	v_add3_u32 v3, v3, v4, s90
	ds_write_b16_d16_hi v2, v3 offset:448
	v_mul_f32_e32 v2, 0x45800000, v1
	v_cndmask_b32_e32 v1, v1, v2, vcc
	v_sub_f32_e32 v3, v23, v0
	v_lshlrev_b32_e32 v2, 10, v212
	v_mul_f32_e32 v3, v3, v1
	v_bfe_u32 v4, v3, 16, 1
	v_add3_u32 v17, 0, v2, v16
	v_sub_f32_e32 v2, v7, v0
	v_add3_u32 v3, v3, v4, s90
	v_mul_f32_e32 v2, v2, v1
	ds_write_b16_d16_hi v17, v3
	v_bfe_u32 v3, v2, 16, 1
	v_add3_u32 v2, v2, v3, s90
	ds_write_b16_d16_hi v17, v2 offset:64
	v_sub_f32_e32 v2, v39, v0
	v_mul_f32_e32 v2, v2, v1
	v_bfe_u32 v3, v2, 16, 1
	v_add3_u32 v2, v2, v3, s90
	ds_write_b16_d16_hi v17, v2 offset:128
	v_sub_f32_e32 v2, v55, v0
	v_mul_f32_e32 v2, v2, v1
	v_bfe_u32 v3, v2, 16, 1
	v_add3_u32 v2, v2, v3, s90
	ds_write_b16_d16_hi v17, v2 offset:192
	v_sub_f32_e32 v2, v103, v0
	v_mul_f32_e32 v2, v2, v1
	v_bfe_u32 v3, v2, 16, 1
	v_add3_u32 v2, v2, v3, s90
	ds_write_b16_d16_hi v17, v2 offset:256
	v_sub_f32_e32 v2, v119, v0
	v_mul_f32_e32 v2, v2, v1
	v_bfe_u32 v3, v2, 16, 1
	v_add3_u32 v2, v2, v3, s90
	ds_write_b16_d16_hi v17, v2 offset:320
	v_sub_f32_e32 v2, v87, v0
	v_sub_f32_e32 v0, v71, v0
	v_mul_f32_e32 v2, v2, v1
	v_mul_f32_e32 v18, v0, v1
	v_lshlrev_b32_e32 v0, 1, v211
	v_bfe_u32 v3, v2, 16, 1
	v_subrev_u32_e32 v0, s6, v0
	v_add3_u32 v2, v2, v3, s90
	v_lshl_add_u32 v0, v0, 2, s4
	ds_write_b16_d16_hi v17, v2 offset:384
	ds_read2_b64 v[0:3], v0 offset0:128 offset1:129
	v_lshlrev_b32_e32 v4, 1, v209
	v_subrev_u32_e32 v4, s6, v4
	v_lshl_add_u32 v4, v4, 2, s4
	ds_read2_b64 v[4:7], v4 offset0:128 offset1:129
	s_waitcnt lgkmcnt(1)
	v_pk_add_f32 v[0:1], v[140:141], v[0:1]
	s_nop 0
	v_pk_mul_f32 v[0:1], v[0:1], s[26:27] op_sel_hi:[1,0]
	s_nop 0
	v_fma_f32 v1, -v0, v0, v1
	v_max_f32_e32 v1, 0, v1
	v_add_f32_e32 v1, 0x358637bd, v1
	v_mul_f32_e32 v19, 0x4b800000, v1
	v_cmp_gt_f32_e32 vcc, s89, v1
	v_sub_f32_e32 v8, v8, v0
	s_nop 0
	v_cndmask_b32_e32 v1, v1, v19, vcc
	v_rsq_f32_e32 v1, v1
	v_bfe_u32 v19, v18, 16, 1
	v_add3_u32 v18, v18, v19, s90
	ds_write_b16_d16_hi v17, v18 offset:448
	v_mul_f32_e32 v17, 0x45800000, v1
	v_cndmask_b32_e32 v1, v1, v17, vcc
	v_sub_f32_e32 v18, v24, v0
	v_mul_f32_e32 v18, v18, v1
	v_lshlrev_b32_e32 v17, 10, v211
	v_bfe_u32 v19, v18, 16, 1
	v_add3_u32 v18, v18, v19, s90
	v_add3_u32 v17, 0, v17, v16
	v_mul_f32_e32 v8, v8, v1
	ds_write_b16_d16_hi v17, v18
	v_bfe_u32 v18, v8, 16, 1
	v_add3_u32 v8, v8, v18, s90
	ds_write_b16_d16_hi v17, v8 offset:64
	v_sub_f32_e32 v8, v40, v0
	v_mul_f32_e32 v8, v8, v1
	v_bfe_u32 v18, v8, 16, 1
	v_add3_u32 v8, v8, v18, s90
	ds_write_b16_d16_hi v17, v8 offset:128
	v_sub_f32_e32 v8, v56, v0
	v_mul_f32_e32 v8, v8, v1
	v_bfe_u32 v18, v8, 16, 1
	v_add3_u32 v8, v8, v18, s90
	ds_write_b16_d16_hi v17, v8 offset:192
	v_sub_f32_e32 v8, v104, v0
	v_mul_f32_e32 v8, v8, v1
	v_bfe_u32 v18, v8, 16, 1
	v_add3_u32 v8, v8, v18, s90
	ds_write_b16_d16_hi v17, v8 offset:256
	v_sub_f32_e32 v8, v120, v0
	v_mul_f32_e32 v8, v8, v1
	v_bfe_u32 v18, v8, 16, 1
	v_add3_u32 v8, v8, v18, s90
	ds_write_b16_d16_hi v17, v8 offset:320
	v_sub_f32_e32 v8, v88, v0
	v_mul_f32_e32 v8, v8, v1
	v_bfe_u32 v18, v8, 16, 1
	v_add3_u32 v8, v8, v18, s90
	v_sub_f32_e32 v0, v72, v0
	ds_write_b16_d16_hi v17, v8 offset:384
	v_mul_f32_e32 v8, v0, v1
	v_pk_add_f32 v[0:1], v[142:143], v[2:3]
	s_nop 0
	v_pk_mul_f32 v[0:1], v[0:1], s[26:27] op_sel_hi:[1,0]
	s_nop 0
	v_fma_f32 v1, -v0, v0, v1
	v_max_f32_e32 v1, 0, v1
	v_add_f32_e32 v1, 0x358637bd, v1
	v_mul_f32_e32 v2, 0x4b800000, v1
	v_cmp_gt_f32_e32 vcc, s89, v1
	v_sub_f32_e32 v3, v25, v0
	s_nop 0
	v_cndmask_b32_e32 v1, v1, v2, vcc
	v_rsq_f32_e32 v1, v1
	v_bfe_u32 v2, v8, 16, 1
	v_add3_u32 v2, v8, v2, s90
	ds_write_b16_d16_hi v17, v2 offset:448
	v_mul_f32_e32 v2, 0x45800000, v1
	v_cndmask_b32_e32 v1, v1, v2, vcc
	v_mul_f32_e32 v3, v3, v1
	v_lshlrev_b32_e32 v2, 10, v210
	v_bfe_u32 v8, v3, 16, 1
	v_add3_u32 v3, v3, v8, s90
	v_add3_u32 v2, 0, v2, v16
	ds_write_b16_d16_hi v2, v3
	v_sub_f32_e32 v3, v9, v0
	v_mul_f32_e32 v3, v3, v1
	v_bfe_u32 v8, v3, 16, 1
	v_add3_u32 v3, v3, v8, s90
	ds_write_b16_d16_hi v2, v3 offset:64
	v_sub_f32_e32 v3, v41, v0
	v_mul_f32_e32 v3, v3, v1
	v_bfe_u32 v8, v3, 16, 1
	v_add3_u32 v3, v3, v8, s90
	ds_write_b16_d16_hi v2, v3 offset:128
	v_sub_f32_e32 v3, v57, v0
	v_mul_f32_e32 v3, v3, v1
	v_bfe_u32 v8, v3, 16, 1
	v_add3_u32 v3, v3, v8, s90
	ds_write_b16_d16_hi v2, v3 offset:192
	v_sub_f32_e32 v3, v105, v0
	v_mul_f32_e32 v3, v3, v1
	v_bfe_u32 v8, v3, 16, 1
	v_add3_u32 v3, v3, v8, s90
	ds_write_b16_d16_hi v2, v3 offset:256
	v_sub_f32_e32 v3, v121, v0
	v_mul_f32_e32 v3, v3, v1
	v_bfe_u32 v8, v3, 16, 1
	v_add3_u32 v3, v3, v8, s90
	ds_write_b16_d16_hi v2, v3 offset:320
	v_sub_f32_e32 v3, v89, v0
	v_mul_f32_e32 v3, v3, v1
	v_bfe_u32 v8, v3, 16, 1
	v_add3_u32 v3, v3, v8, s90
	v_sub_f32_e32 v0, v73, v0
	ds_write_b16_d16_hi v2, v3 offset:384
	v_mul_f32_e32 v3, v0, v1
	s_waitcnt lgkmcnt(14)
; #define LAS __attribute__((address_space(3)))
; __device__ __forceinline__ bf16_t f2bf(float f) { unsigned u = __builtin_bit_cast(unsigned, f); return (bf16_t)((u + 0x7fffu + ((u >> 16) & 1u)) >> 16); }
; __device__ __forceinline__ int crow(int r, int hi) { return (r & 3) + 8 * (r >> 2) + 4 * hi; }
; __device__ __forceinline__ int crow(int r, int hi) { return (r & 3) + 8 * (r >> 2) + 4 * hi; }
; template <int DK, int DV, bool MLSTM>
; __device__ __forceinline__ void out_unit2(LAS unsigned char* lds, LAS unsigned char* ldstab, const OutArgs a, const int wv) {
;     ...
;     for (int r = 0; r < 16; ++r) {
;         const int row = 32 * rb + crow(r, hi);
;         const float t1 = s1[r] + exch[((1 - dh) * 128 + row) * 2], t2 = s2[r] + exch[((1 - dh) * 128 + row) * 2 + 1];
;         float mean, inv;
;         if (MLSTM) { mean = 0.f; inv = rsqrtf(t2 * (1.f / DV) + EPS); }
;         else { mean = t1 * (1.f / DV); inv = rsqrtf(fmaxf(t2 * (1.f / DV) - mean * mean, 0.f) + EPS); }
; #pragma unroll
;         for (int nb = 0; nb < NB; ++nb) { const int col = dh * (DV / 2) + 32 * nb + r32;
;             *(LAS bf16_t*)(lds + row * TP + col * 2) = f2bf((o[nb][r] - mean) * inv); }
	v_pk_add_f32 v[0:1], v[136:137], v[4:5]
	s_nop 0
	v_pk_mul_f32 v[0:1], v[0:1], s[26:27] op_sel_hi:[1,0]
	s_nop 0
	v_fma_f32 v1, -v0, v0, v1
	v_max_f32_e32 v1, 0, v1
	v_add_f32_e32 v1, 0x358637bd, v1
	v_mul_f32_e32 v4, 0x4b800000, v1
	v_cmp_gt_f32_e32 vcc, s89, v1
	s_nop 1
	v_cndmask_b32_e32 v1, v1, v4, vcc
	v_rsq_f32_e32 v1, v1
	v_bfe_u32 v4, v3, 16, 1
	v_add3_u32 v3, v3, v4, s90
	ds_write_b16_d16_hi v2, v3 offset:448
	v_mul_f32_e32 v2, 0x45800000, v1
	v_cndmask_b32_e32 v1, v1, v2, vcc
	v_sub_f32_e32 v3, v26, v0
	v_mul_f32_e32 v3, v3, v1
	v_lshlrev_b32_e32 v2, 10, v209
	v_bfe_u32 v4, v3, 16, 1
	v_add3_u32 v3, v3, v4, s90
	v_add3_u32 v2, 0, v2, v16
	ds_write_b16_d16_hi v2, v3
	v_sub_f32_e32 v3, v10, v0
	v_mul_f32_e32 v3, v3, v1
	v_bfe_u32 v4, v3, 16, 1
	v_add3_u32 v3, v3, v4, s90
	ds_write_b16_d16_hi v2, v3 offset:64
	v_sub_f32_e32 v3, v42, v0
	v_mul_f32_e32 v3, v3, v1
	v_bfe_u32 v4, v3, 16, 1
	v_add3_u32 v3, v3, v4, s90
	ds_write_b16_d16_hi v2, v3 offset:128
	v_sub_f32_e32 v3, v58, v0
	v_mul_f32_e32 v3, v3, v1
	v_bfe_u32 v4, v3, 16, 1
	v_add3_u32 v3, v3, v4, s90
	ds_write_b16_d16_hi v2, v3 offset:192
	v_sub_f32_e32 v3, v106, v0
	v_mul_f32_e32 v3, v3, v1
	v_bfe_u32 v4, v3, 16, 1
	v_add3_u32 v3, v3, v4, s90
	ds_write_b16_d16_hi v2, v3 offset:256
	v_sub_f32_e32 v3, v122, v0
	v_mul_f32_e32 v3, v3, v1
	v_bfe_u32 v4, v3, 16, 1
	v_add3_u32 v3, v3, v4, s90
	ds_write_b16_d16_hi v2, v3 offset:320
	v_sub_f32_e32 v3, v90, v0
	v_mul_f32_e32 v3, v3, v1
	v_bfe_u32 v4, v3, 16, 1
	v_add3_u32 v3, v3, v4, s90
	v_sub_f32_e32 v0, v74, v0
	ds_write_b16_d16_hi v2, v3 offset:384
	v_mul_f32_e32 v3, v0, v1
	v_pk_add_f32 v[0:1], v[138:139], v[6:7]
	s_nop 0
	v_pk_mul_f32 v[0:1], v[0:1], s[26:27] op_sel_hi:[1,0]
	s_nop 0
	v_fma_f32 v1, -v0, v0, v1
	v_max_f32_e32 v1, 0, v1
	v_add_f32_e32 v1, 0x358637bd, v1
	v_mul_f32_e32 v4, 0x4b800000, v1
	v_cmp_gt_f32_e32 vcc, s89, v1
	s_nop 1
	v_cndmask_b32_e32 v1, v1, v4, vcc
	v_rsq_f32_e32 v1, v1
	v_bfe_u32 v4, v3, 16, 1
	v_add3_u32 v3, v3, v4, s90
	ds_write_b16_d16_hi v2, v3 offset:448
	v_mul_f32_e32 v2, 0x45800000, v1
	v_cndmask_b32_e32 v1, v1, v2, vcc
	v_sub_f32_e32 v3, v27, v0
	v_lshlrev_b32_e32 v2, 10, v208
	v_mul_f32_e32 v3, v3, v1
	v_bfe_u32 v4, v3, 16, 1
	v_add3_u32 v8, 0, v2, v16
	v_sub_f32_e32 v2, v11, v0
	v_add3_u32 v3, v3, v4, s90
	v_mul_f32_e32 v2, v2, v1
	ds_write_b16_d16_hi v8, v3
	v_bfe_u32 v3, v2, 16, 1
	v_add3_u32 v2, v2, v3, s90
	ds_write_b16_d16_hi v8, v2 offset:64
	v_sub_f32_e32 v2, v43, v0
	v_mul_f32_e32 v2, v2, v1
	v_bfe_u32 v3, v2, 16, 1
	v_add3_u32 v2, v2, v3, s90
	ds_write_b16_d16_hi v8, v2 offset:128
	v_sub_f32_e32 v2, v59, v0
	v_mul_f32_e32 v2, v2, v1
	v_bfe_u32 v3, v2, 16, 1
	v_add3_u32 v2, v2, v3, s90
	ds_write_b16_d16_hi v8, v2 offset:192
	v_sub_f32_e32 v2, v107, v0
	v_mul_f32_e32 v2, v2, v1
	v_bfe_u32 v3, v2, 16, 1
	v_add3_u32 v2, v2, v3, s90
	ds_write_b16_d16_hi v8, v2 offset:256
	v_sub_f32_e32 v2, v123, v0
	v_mul_f32_e32 v2, v2, v1
	v_bfe_u32 v3, v2, 16, 1
	v_add3_u32 v2, v2, v3, s90
	ds_write_b16_d16_hi v8, v2 offset:320
	v_sub_f32_e32 v2, v91, v0
	v_sub_f32_e32 v0, v75, v0
	v_mul_f32_e32 v2, v2, v1
	v_mul_f32_e32 v9, v0, v1
	v_lshlrev_b32_e32 v0, 1, v207
	v_bfe_u32 v3, v2, 16, 1
	v_subrev_u32_e32 v0, s6, v0
	v_add3_u32 v2, v2, v3, s90
	v_lshl_add_u32 v0, v0, 2, s4
	ds_write_b16_d16_hi v8, v2 offset:384
	ds_read2_b64 v[0:3], v0 offset0:128 offset1:129
	v_lshlrev_b32_e32 v4, 1, v162
	v_subrev_u32_e32 v4, s6, v4
	v_lshl_add_u32 v4, v4, 2, s4
	ds_read2_b64 v[4:7], v4 offset0:128 offset1:129
	s_waitcnt lgkmcnt(1)
	v_pk_add_f32 v[0:1], v[132:133], v[0:1]
	s_nop 0
	v_pk_mul_f32 v[0:1], v[0:1], s[26:27] op_sel_hi:[1,0]
	s_nop 0
	v_fma_f32 v1, -v0, v0, v1
	v_max_f32_e32 v1, 0, v1
	v_add_f32_e32 v1, 0x358637bd, v1
	v_mul_f32_e32 v10, 0x4b800000, v1
	v_cmp_gt_f32_e32 vcc, s89, v1
	s_nop 1
	v_cndmask_b32_e32 v1, v1, v10, vcc
	v_rsq_f32_e32 v1, v1
	v_bfe_u32 v10, v9, 16, 1
	v_add3_u32 v9, v9, v10, s90
	ds_write_b16_d16_hi v8, v9 offset:448
	v_mul_f32_e32 v8, 0x45800000, v1
	v_cndmask_b32_e32 v1, v1, v8, vcc
	v_sub_f32_e32 v9, v28, v0
	v_mul_f32_e32 v9, v9, v1
	v_lshlrev_b32_e32 v8, 10, v207
	v_bfe_u32 v10, v9, 16, 1
	v_add3_u32 v9, v9, v10, s90
	v_add3_u32 v8, 0, v8, v16
	ds_write_b16_d16_hi v8, v9
	v_sub_f32_e32 v9, v12, v0
	v_mul_f32_e32 v9, v9, v1
	v_bfe_u32 v10, v9, 16, 1
	v_add3_u32 v9, v9, v10, s90
	ds_write_b16_d16_hi v8, v9 offset:64
	v_sub_f32_e32 v9, v44, v0
	v_mul_f32_e32 v9, v9, v1
	v_bfe_u32 v10, v9, 16, 1
	v_add3_u32 v9, v9, v10, s90
	ds_write_b16_d16_hi v8, v9 offset:128
	v_sub_f32_e32 v9, v60, v0
	v_mul_f32_e32 v9, v9, v1
	v_bfe_u32 v10, v9, 16, 1
	v_add3_u32 v9, v9, v10, s90
	ds_write_b16_d16_hi v8, v9 offset:192
	v_sub_f32_e32 v9, v108, v0
	v_mul_f32_e32 v9, v9, v1
	v_bfe_u32 v10, v9, 16, 1
	v_add3_u32 v9, v9, v10, s90
	ds_write_b16_d16_hi v8, v9 offset:256
	v_sub_f32_e32 v9, v124, v0
	v_mul_f32_e32 v9, v9, v1
	v_bfe_u32 v10, v9, 16, 1
	v_add3_u32 v9, v9, v10, s90
	ds_write_b16_d16_hi v8, v9 offset:320
	v_sub_f32_e32 v9, v92, v0
	v_mul_f32_e32 v9, v9, v1
	v_bfe_u32 v10, v9, 16, 1
	v_add3_u32 v9, v9, v10, s90
	v_sub_f32_e32 v0, v76, v0
	ds_write_b16_d16_hi v8, v9 offset:384
	v_mul_f32_e32 v9, v0, v1
	v_pk_add_f32 v[0:1], v[134:135], v[2:3]
	s_nop 0
	v_pk_mul_f32 v[0:1], v[0:1], s[26:27] op_sel_hi:[1,0]
	s_nop 0
	v_fma_f32 v1, -v0, v0, v1
	v_max_f32_e32 v1, 0, v1
	v_add_f32_e32 v1, 0x358637bd, v1
	v_mul_f32_e32 v2, 0x4b800000, v1
	v_cmp_gt_f32_e32 vcc, s89, v1
	v_sub_f32_e32 v3, v29, v0
	s_nop 0
	v_cndmask_b32_e32 v1, v1, v2, vcc
	v_rsq_f32_e32 v1, v1
	v_bfe_u32 v2, v9, 16, 1
	v_add3_u32 v2, v9, v2, s90
	ds_write_b16_d16_hi v8, v2 offset:448
	v_mul_f32_e32 v2, 0x45800000, v1
	v_cndmask_b32_e32 v1, v1, v2, vcc
	v_mul_f32_e32 v3, v3, v1
	v_lshlrev_b32_e32 v2, 10, v206
	v_bfe_u32 v8, v3, 16, 1
	v_add3_u32 v3, v3, v8, s90
	v_add3_u32 v2, 0, v2, v16
	ds_write_b16_d16_hi v2, v3
	v_sub_f32_e32 v3, v13, v0
	v_mul_f32_e32 v3, v3, v1
	v_bfe_u32 v8, v3, 16, 1
	v_add3_u32 v3, v3, v8, s90
	ds_write_b16_d16_hi v2, v3 offset:64
	v_sub_f32_e32 v3, v45, v0
	v_mul_f32_e32 v3, v3, v1
	v_bfe_u32 v8, v3, 16, 1
	v_add3_u32 v3, v3, v8, s90
	ds_write_b16_d16_hi v2, v3 offset:128
	v_sub_f32_e32 v3, v61, v0
	v_mul_f32_e32 v3, v3, v1
	v_bfe_u32 v8, v3, 16, 1
	v_add3_u32 v3, v3, v8, s90
	ds_write_b16_d16_hi v2, v3 offset:192
	v_sub_f32_e32 v3, v109, v0
	v_mul_f32_e32 v3, v3, v1
	v_bfe_u32 v8, v3, 16, 1
	v_add3_u32 v3, v3, v8, s90
	ds_write_b16_d16_hi v2, v3 offset:256
	v_sub_f32_e32 v3, v125, v0
	v_mul_f32_e32 v3, v3, v1
	v_bfe_u32 v8, v3, 16, 1
	v_add3_u32 v3, v3, v8, s90
	ds_write_b16_d16_hi v2, v3 offset:320
	v_sub_f32_e32 v3, v93, v0
	v_mul_f32_e32 v3, v3, v1
	v_bfe_u32 v8, v3, 16, 1
	v_add3_u32 v3, v3, v8, s90
	v_sub_f32_e32 v0, v77, v0
	ds_write_b16_d16_hi v2, v3 offset:384
	v_mul_f32_e32 v3, v0, v1
	s_waitcnt lgkmcnt(14)
; #define LAS __attribute__((address_space(3)))
; __device__ __forceinline__ bf16_t f2bf(float f) { unsigned u = __builtin_bit_cast(unsigned, f); return (bf16_t)((u + 0x7fffu + ((u >> 16) & 1u)) >> 16); }
; __device__ __forceinline__ int crow(int r, int hi) { return (r & 3) + 8 * (r >> 2) + 4 * hi; }
; __device__ __forceinline__ int crow(int r, int hi) { return (r & 3) + 8 * (r >> 2) + 4 * hi; }
; template <int DK, int DV, bool MLSTM>
; __device__ __forceinline__ void out_unit2(LAS unsigned char* lds, LAS unsigned char* ldstab, const OutArgs a, const int wv) {
;     ...
;     for (int r = 0; r < 16; ++r) {
;         const int row = 32 * rb + crow(r, hi);
;         const float t1 = s1[r] + exch[((1 - dh) * 128 + row) * 2], t2 = s2[r] + exch[((1 - dh) * 128 + row) * 2 + 1];
;         float mean, inv;
;         if (MLSTM) { mean = 0.f; inv = rsqrtf(t2 * (1.f / DV) + EPS); }
;         else { mean = t1 * (1.f / DV); inv = rsqrtf(fmaxf(t2 * (1.f / DV) - mean * mean, 0.f) + EPS); }
; #pragma unroll
;         for (int nb = 0; nb < NB; ++nb) { const int col = dh * (DV / 2) + 32 * nb + r32;
;             *(LAS bf16_t*)(lds + row * TP + col * 2) = f2bf((o[nb][r] - mean) * inv); }
;     }
;     __syncthreads();
;     constexpr int CPR = DV / 8;
; #pragma unroll 1
;     for (int id = tid; id < 128 * CPR; id += 512) { const int row = id / CPR, ch = id % CPR;
;         const u32x4 y = *(const LAS u32x4*)(lds + row * TP + ch * 16);
;         const f32x4 g0 = *(const f32x4*)(a.gain + 8 * ch), g1 = *(const f32x4*)(a.gain + 8 * ch + 4);
	v_pk_add_f32 v[0:1], v[128:129], v[4:5]
	s_nop 0
	v_pk_mul_f32 v[0:1], v[0:1], s[26:27] op_sel_hi:[1,0]
	s_nop 0
	v_fma_f32 v1, -v0, v0, v1
	v_max_f32_e32 v1, 0, v1
	v_add_f32_e32 v1, 0x358637bd, v1
	v_mul_f32_e32 v4, 0x4b800000, v1
	v_cmp_gt_f32_e32 vcc, s89, v1
	s_nop 1
	v_cndmask_b32_e32 v1, v1, v4, vcc
	v_rsq_f32_e32 v1, v1
	v_bfe_u32 v4, v3, 16, 1
	v_add3_u32 v3, v3, v4, s90
	ds_write_b16_d16_hi v2, v3 offset:448
	v_mul_f32_e32 v2, 0x45800000, v1
	v_cndmask_b32_e32 v1, v1, v2, vcc
	v_sub_f32_e32 v3, v30, v0
	v_mul_f32_e32 v3, v3, v1
	v_lshlrev_b32_e32 v2, 10, v162
	v_bfe_u32 v4, v3, 16, 1
	v_add3_u32 v3, v3, v4, s90
	v_add3_u32 v2, 0, v2, v16
	ds_write_b16_d16_hi v2, v3
	v_sub_f32_e32 v3, v14, v0
	v_mul_f32_e32 v3, v3, v1
	v_bfe_u32 v4, v3, 16, 1
	v_add3_u32 v3, v3, v4, s90
	ds_write_b16_d16_hi v2, v3 offset:64
	v_sub_f32_e32 v3, v46, v0
	v_mul_f32_e32 v3, v3, v1
	v_bfe_u32 v4, v3, 16, 1
	v_add3_u32 v3, v3, v4, s90
	ds_write_b16_d16_hi v2, v3 offset:128
	v_sub_f32_e32 v3, v62, v0
	v_mul_f32_e32 v3, v3, v1
	v_bfe_u32 v4, v3, 16, 1
	v_add3_u32 v3, v3, v4, s90
	ds_write_b16_d16_hi v2, v3 offset:192
	v_sub_f32_e32 v3, v110, v0
	v_mul_f32_e32 v3, v3, v1
	v_bfe_u32 v4, v3, 16, 1
	v_add3_u32 v3, v3, v4, s90
	ds_write_b16_d16_hi v2, v3 offset:256
	v_sub_f32_e32 v3, v126, v0
	v_mul_f32_e32 v3, v3, v1
	v_bfe_u32 v4, v3, 16, 1
	v_add3_u32 v3, v3, v4, s90
	ds_write_b16_d16_hi v2, v3 offset:320
	v_sub_f32_e32 v3, v94, v0
	v_mul_f32_e32 v3, v3, v1
	v_bfe_u32 v4, v3, 16, 1
	v_add3_u32 v3, v3, v4, s90
	v_sub_f32_e32 v0, v78, v0
	ds_write_b16_d16_hi v2, v3 offset:384
	v_mul_f32_e32 v3, v0, v1
	v_pk_add_f32 v[0:1], v[130:131], v[6:7]
	s_nop 0
	v_pk_mul_f32 v[0:1], v[0:1], s[26:27] op_sel_hi:[1,0]
	s_nop 0
	v_fma_f32 v1, -v0, v0, v1
	v_max_f32_e32 v1, 0, v1
	v_add_f32_e32 v1, 0x358637bd, v1
	v_mul_f32_e32 v4, 0x4b800000, v1
	v_cmp_gt_f32_e32 vcc, s89, v1
	s_nop 1
	v_cndmask_b32_e32 v1, v1, v4, vcc
	v_rsq_f32_e32 v1, v1
	v_bfe_u32 v4, v3, 16, 1
	v_add3_u32 v3, v3, v4, s90
	ds_write_b16_d16_hi v2, v3 offset:448
	v_mul_f32_e32 v2, 0x45800000, v1
	v_cndmask_b32_e32 v1, v1, v2, vcc
	v_sub_f32_e32 v3, v31, v0
	v_mul_f32_e32 v3, v3, v1
	v_lshlrev_b32_e32 v2, 10, v160
	v_bfe_u32 v4, v3, 16, 1
	v_add3_u32 v3, v3, v4, s90
	v_add3_u32 v2, 0, v2, v16
	ds_write_b16_d16_hi v2, v3
	v_sub_f32_e32 v3, v15, v0
	v_mul_f32_e32 v3, v3, v1
	v_bfe_u32 v4, v3, 16, 1
	v_add3_u32 v3, v3, v4, s90
	ds_write_b16_d16_hi v2, v3 offset:64
	v_sub_f32_e32 v3, v47, v0
	v_mul_f32_e32 v3, v3, v1
	v_bfe_u32 v4, v3, 16, 1
	v_add3_u32 v3, v3, v4, s90
	ds_write_b16_d16_hi v2, v3 offset:128
	v_sub_f32_e32 v3, v63, v0
	v_mul_f32_e32 v3, v3, v1
	v_bfe_u32 v4, v3, 16, 1
	v_add3_u32 v3, v3, v4, s90
	ds_write_b16_d16_hi v2, v3 offset:192
	v_sub_f32_e32 v3, v111, v0
	v_mul_f32_e32 v3, v3, v1
	v_bfe_u32 v4, v3, 16, 1
	v_add3_u32 v3, v3, v4, s90
	ds_write_b16_d16_hi v2, v3 offset:256
	v_sub_f32_e32 v3, v127, v0
	v_mul_f32_e32 v3, v3, v1
	v_bfe_u32 v4, v3, 16, 1
	v_add3_u32 v3, v3, v4, s90
	ds_write_b16_d16_hi v2, v3 offset:320
	v_sub_f32_e32 v3, v95, v0
	v_sub_f32_e32 v0, v79, v0
	v_mul_f32_e32 v3, v3, v1
	v_mul_f32_e32 v0, v0, v1
	v_bfe_u32 v4, v3, 16, 1
	v_bfe_u32 v1, v0, 16, 1
	v_add3_u32 v3, v3, v4, s90
	v_add3_u32 v0, v0, v1, s90
	v_cmp_gt_i32_e32 vcc, s88, v232
	ds_write_b16_d16_hi v2, v3 offset:384
	ds_write_b16_d16_hi v2, v0 offset:448
	s_waitcnt lgkmcnt(0)
	s_barrier
	s_and_saveexec_b64 s[36:37], vcc
	s_cbranch_execz .LBB0_4301
	s_lshl_b32 s4, s8, 2
	s_add_u32 s38, s51, s4
	s_addc_u32 s39, s52, 0
	s_lshl_b64 s[2:3], s[2:3], 11
	s_add_u32 s4, s53, s2
	s_addc_u32 s5, s54, s3
	s_add_u32 s40, s4, s8
	s_addc_u32 s41, s5, 0
	s_add_u32 s2, s55, s2
	s_addc_u32 s3, s56, s3
	s_add_u32 s42, s2, s8
	s_addc_u32 s43, s3, 0
	v_lshl_add_u32 v4, v232, 4, 0
	v_lshlrev_b32_e32 v5, 3, v232
	s_mov_b64 s[44:45], 0
	v_and_b32_e32 v6, 63, v232
	v_lshrrev_b32_e32 v7, 6, v232
	v_lshlrev_b32_e32 v8, 5, v6
	v_lshlrev_b32_e32 v5, 3, v6
	v_lshl_add_u32 v5, v7, 11, v5
	global_load_dwordx4 v[40:43], v8, s[38:39]
	global_load_dwordx4 v[44:47], v8, s[38:39] offset:16
	v_mov_b32_e32 v162, v163
	s_movk_i32 s44, 16
; #define LAS __attribute__((address_space(3)))
; __device__ __forceinline__ float sigmoidf_(float x) { return 1.f / (1.f + __expf(-x)); }
; __device__ __forceinline__ float siluf_(float x) { return x / (1.f + __expf(-x)); }
; template <int DK, int DV, bool MLSTM>
; __device__ __forceinline__ void out_unit2(LAS unsigned char* lds, LAS unsigned char* ldstab, const OutArgs a, const int wv) {
;     ...
; #pragma unroll 1
;     for (int id = tid; id < 128 * CPR; id += 512) { const int row = id / CPR, ch = id % CPR;
;         const u32x4 y = *(const LAS u32x4*)(lds + row * TP + ch * 16);
;         const f32x4 g0 = *(const f32x4*)(a.gain + 8 * ch), g1 = *(const f32x4*)(a.gain + 8 * ch + 4);
;         float yv[8] = {bf_lo(y.x), bf_hi(y.x), bf_lo(y.y), bf_hi(y.y), bf_lo(y.z), bf_hi(y.z), bf_lo(y.w), bf_hi(y.w)};
;         float gv[8];
;         if (MLSTM) { const u32x4 g = *(const u32x4*)(a.G + (size_t)row * a.ldg + 8 * ch);
;             gv[0] = bf_lo(g.x); gv[1] = bf_hi(g.x); gv[2] = bf_lo(g.y); gv[3] = bf_hi(g.y); gv[4] = bf_lo(g.z); gv[5] = bf_hi(g.z); gv[6] = bf_lo(g.w); gv[7] = bf_hi(g.w); }
;         else { const u32x2 g = *(const u32x2*)(a.G8 + (size_t)row * a.ldg8 + 8 * ch);
;             const f32x2 e0 = __builtin_amdgcn_cvt_pk_f32_fp8((int)g.x, false), e1 = __builtin_amdgcn_cvt_pk_f32_fp8((int)g.x, true), e2 = __builtin_amdgcn_cvt_pk_f32_fp8((int)g.y, false), e3 = __builtin_amdgcn_cvt_pk_f32_fp8((int)g.y, true);
;             gv[0] = e0[0] * a.g8inv; gv[1] = e0[1] * a.g8inv; gv[2] = e1[0] * a.g8inv; gv[3] = e1[1] * a.g8inv; gv[4] = e2[0] * a.g8inv; gv[5] = e2[1] * a.g8inv; gv[6] = e3[0] * a.g8inv; gv[7] = e3[1] * a.g8inv; }
;         float gn[8] = {g0[0], g0[1], g0[2], g0[3], g1[0], g1[1], g1[2], g1[3]};
;         float ov[8];
; #pragma unroll
;         for (int i = 0; i < 8; ++i) ov[i] = yv[i] * gn[i] * (MLSTM ? sigmoidf_(gv[i]) : siluf_(gv[i]));
;         u32x2 w; w.x = pg8::pk4_fp8c(ov[0] * a.oscale, ov[1] * a.oscale, ov[2] * a.oscale, ov[3] * a.oscale); w.y = pg8::pk4_fp8c(ov[4] * a.oscale, ov[5] * a.oscale, ov[6] * a.oscale, ov[7] * a.oscale);
;         *(u32x2*)(a.Out + (size_t)row * a.ldo + 8 * ch) = w; }
.Ldloop1:
	ds_read_b128 v[0:3], v4
	global_load_dwordx2 v[30:31], v5, s[40:41]
	v_add_u32_e32 v4, 0x2000, v4
	s_waitcnt lgkmcnt(0)
	v_lshlrev_b32_e32 v10, 16, v0
	v_and_b32_e32 v11, 0xffff0000, v0
	v_lshlrev_b32_e32 v12, 16, v1
	v_and_b32_e32 v13, 0xffff0000, v1
	v_lshlrev_b32_e32 v14, 16, v2
	v_and_b32_e32 v15, 0xffff0000, v2
	v_lshlrev_b32_e32 v16, 16, v3
	v_and_b32_e32 v17, 0xffff0000, v3
	s_waitcnt vmcnt(0)
	v_cvt_pk_f32_fp8_e32 v[32:33], v30
	v_cvt_pk_f32_fp8_sdwa v[34:35], v30 src0_sel:WORD_1
	v_cvt_pk_f32_fp8_e32 v[36:37], v31
	v_cvt_pk_f32_fp8_sdwa v[38:39], v31 src0_sel:WORD_1
	v_pk_mul_f32 v[10:11], v[40:41], v[10:11]
	v_pk_mul_f32 v[12:13], v[42:43], v[12:13]
	v_pk_mul_f32 v[14:15], v[44:45], v[14:15]
	v_pk_mul_f32 v[16:17], v[46:47], v[16:17]
	v_pk_mul_f32 v[32:33], v[32:33], v[162:163]
	v_pk_mul_f32 v[34:35], v[34:35], v[162:163]
	v_pk_mul_f32 v[36:37], v[36:37], v[162:163]
	v_pk_mul_f32 v[38:39], v[38:39], v[162:163]
	v_mul_f32_e32 v48, 0xbfb8aa3b, v32
	v_mul_f32_e32 v49, 0xbfb8aa3b, v33
	v_mul_f32_e32 v50, 0xbfb8aa3b, v34
	v_mul_f32_e32 v51, 0xbfb8aa3b, v35
	v_mul_f32_e32 v52, 0xbfb8aa3b, v36
	v_mul_f32_e32 v53, 0xbfb8aa3b, v37
	v_mul_f32_e32 v54, 0xbfb8aa3b, v38
	v_mul_f32_e32 v55, 0xbfb8aa3b, v39
	v_exp_f32_e32 v48, v48
	v_exp_f32_e32 v49, v49
	v_exp_f32_e32 v50, v50
	v_exp_f32_e32 v51, v51
	v_exp_f32_e32 v52, v52
	v_exp_f32_e32 v53, v53
	v_exp_f32_e32 v54, v54
	v_exp_f32_e32 v55, v55
	v_add_f32_e32 v48, 1.0, v48
	v_add_f32_e32 v49, 1.0, v49
	v_add_f32_e32 v50, 1.0, v50
	v_add_f32_e32 v51, 1.0, v51
	v_add_f32_e32 v52, 1.0, v52
	v_add_f32_e32 v53, 1.0, v53
	v_add_f32_e32 v54, 1.0, v54
	v_add_f32_e32 v55, 1.0, v55
	v_rcp_f32_e32 v56, v48
	v_rcp_f32_e32 v57, v49
	v_rcp_f32_e32 v58, v50
	v_rcp_f32_e32 v59, v51
	v_rcp_f32_e32 v60, v52
	v_rcp_f32_e32 v61, v53
	v_rcp_f32_e32 v62, v54
	v_rcp_f32_e32 v63, v55
	v_fma_f32 v0, -v48, v56, 1.0
	v_fma_f32 v1, -v49, v57, 1.0
	v_fma_f32 v2, -v50, v58, 1.0
	v_fma_f32 v3, -v51, v59, 1.0
	v_fma_f32 v6, -v52, v60, 1.0
	v_fma_f32 v7, -v53, v61, 1.0
	v_fma_f32 v8, -v54, v62, 1.0
	v_fma_f32 v9, -v55, v63, 1.0
	v_fmac_f32_e32 v56, v0, v56
	v_fmac_f32_e32 v57, v1, v57
	v_fmac_f32_e32 v58, v2, v58
	v_fmac_f32_e32 v59, v3, v59
	v_fmac_f32_e32 v60, v6, v60
	v_fmac_f32_e32 v61, v7, v61
	v_fmac_f32_e32 v62, v8, v62
	v_fmac_f32_e32 v63, v9, v63
	v_mul_f32_e32 v64, v32, v56
	v_mul_f32_e32 v65, v33, v57
	v_mul_f32_e32 v66, v34, v58
	v_mul_f32_e32 v67, v35, v59
	v_mul_f32_e32 v68, v36, v60
	v_mul_f32_e32 v69, v37, v61
	v_mul_f32_e32 v70, v38, v62
	v_mul_f32_e32 v71, v39, v63
	v_fma_f32 v0, -v48, v64, v32
	v_fma_f32 v1, -v49, v65, v33
	v_fma_f32 v2, -v50, v66, v34
	v_fma_f32 v3, -v51, v67, v35
	v_fma_f32 v6, -v52, v68, v36
	v_fma_f32 v7, -v53, v69, v37
	v_fma_f32 v8, -v54, v70, v38
	v_fma_f32 v9, -v55, v71, v39
	v_fmac_f32_e32 v64, v0, v56
	v_fmac_f32_e32 v65, v1, v57
	v_fmac_f32_e32 v66, v2, v58
	v_fmac_f32_e32 v67, v3, v59
	v_fmac_f32_e32 v68, v6, v60
	v_fmac_f32_e32 v69, v7, v61
	v_fmac_f32_e32 v70, v8, v62
	v_fmac_f32_e32 v71, v9, v63
	v_fma_f32 v0, -v48, v64, v32
	v_fma_f32 v1, -v49, v65, v33
	v_fma_f32 v2, -v50, v66, v34
	v_fma_f32 v3, -v51, v67, v35
	v_fma_f32 v6, -v52, v68, v36
	v_fma_f32 v7, -v53, v69, v37
	v_fma_f32 v8, -v54, v70, v38
	v_fma_f32 v9, -v55, v71, v39
	v_fma_f32 v0, v0, v56, v64
	v_fma_f32 v1, v1, v57, v65
	v_fma_f32 v2, v2, v58, v66
	v_fma_f32 v3, v3, v59, v67
	v_fma_f32 v6, v6, v60, v68
	v_fma_f32 v7, v7, v61, v69
	v_fma_f32 v8, v8, v62, v70
	v_fma_f32 v9, v9, v63, v71
	v_div_fixup_f32 v0, v0, v48, v32
	v_div_fixup_f32 v1, v1, v49, v33
	v_div_fixup_f32 v2, v2, v50, v34
	v_div_fixup_f32 v3, v3, v51, v35
	v_div_fixup_f32 v6, v6, v52, v36
	v_div_fixup_f32 v7, v7, v53, v37
	v_div_fixup_f32 v8, v8, v54, v38
	v_div_fixup_f32 v9, v9, v55, v39
	v_mul_f32_e32 v10, v10, v0
	v_mul_f32_e32 v11, v11, v1
	v_mul_f32_e32 v12, v12, v2
	v_mul_f32_e32 v13, v13, v3
	v_mul_f32_e32 v14, v14, v6
	v_mul_f32_e32 v15, v15, v7
	v_mul_f32_e32 v16, v16, v8
	v_mul_f32_e32 v17, v17, v9
	v_mul_f32_e32 v10, 0x41800000, v10
	v_mul_f32_e32 v11, 0x41800000, v11
	v_mul_f32_e32 v12, 0x41800000, v12
	v_mul_f32_e32 v13, 0x41800000, v13
	v_mul_f32_e32 v14, 0x41800000, v14
	v_mul_f32_e32 v15, 0x41800000, v15
	v_mul_f32_e32 v16, 0x41800000, v16
	v_mul_f32_e32 v17, 0x41800000, v17
	v_med3_f32 v10, v10, s91, v231
	v_med3_f32 v11, v11, s91, v231
	v_med3_f32 v12, v12, s91, v231
	v_med3_f32 v13, v13, s91, v231
	v_med3_f32 v14, v14, s91, v231
	v_med3_f32 v15, v15, s91, v231
	v_med3_f32 v16, v16, s91, v231
	v_med3_f32 v17, v17, s91, v231
	v_cvt_pk_fp8_f32 v24, v10, v11
	v_cvt_pk_fp8_f32 v25, v14, v15
	s_nop 0
	v_cvt_pk_fp8_f32 v24, v12, v13 op_sel:[0,0,1]
	v_cvt_pk_fp8_f32 v25, v16, v17 op_sel:[0,0,1]
	s_add_i32 s44, s44, -1
	s_cmp_lg_u32 s44, 0
	s_nop 0
	global_store_dwordx2 v5, v[24:25], s[42:43]
	v_add_u32_e32 v5, 0x4000, v5
	s_cbranch_scc1 .Ldloop1
	s_branch .LBB0_4301
